# plan M: all set-aside conversion workgroups (in-proj-0, out-proj-0, MoE-up-0, in-proj-1) run the hand-written f32->fp8 conversion routine; ranges as plan E
# baseline (speedup 1.0000x reference)
.LBB0_462:
	s_load_dwordx4 s[0:3], s[8:9], 0x138
	s_waitcnt lgkmcnt(0)
	s_mov_b64 s[4:5], s[0:1]
	s_cmp_lt_i32 s4, 5
	s_cselect_b64 s[0:1], -1, 0
	s_cmp_gt_i32 s5, 4
	s_cselect_b64 s[2:3], -1, 0
	s_and_b64 s[0:1], s[0:1], s[2:3]
	s_andn2_b64 vcc, exec, s[0:1]
	s_cbranch_vccnz .LBB0_559
	s_mov_b64 s[0:1], s[8:9]
	v_mbcnt_lo_u32_b32 v156, -1, 0
	v_mbcnt_hi_u32_b32 v156, -1, v156
	s_load_dword s56, s[8:9], 0x148
	s_add_u32 s4, s8, 0x148
	v_readlane_b32 s2, v243, 0
	s_addc_u32 s5, s9, 0
	v_readlane_b32 s3, v243, 1
	s_waitcnt lgkmcnt(0)
	s_sub_i32 s57, s56, 64
	s_cmp_lt_i32 s2, s57
	s_mov_b64 s[2:3], -1
	s_cbranch_scc1 .LBB0_485
	s_mov_b64 s[30:31], s[4:5]
	v_readlane_b32 s4, v243, 0
	s_sub_i32 s4, s4, s57
	s_lshl_b32 s4, s4, 3
	s_add_i32 s19, s4, s94
	s_mov_b32 s4, s19
	s_mov_b32 s5, 0x200
	s_mov_b32 s6, 0x2400
	s_waitcnt vmcnt(0)
	s_cmp_ge_u32 s4, s6
	s_cbranch_scc1 .Lp4c0_done
	v_readlane_b32 s8, v243, 7
	v_readlane_b32 s9, v243, 8
	s_load_dwordx2 s[10:11], s[8:9], 0x130
	s_load_dwordx2 s[12:13], s[8:9], 0xf8
	s_load_dwordx2 s[14:15], s[8:9], 0x108
	v_mbcnt_lo_u32_b32 v172, -1, 0
	v_mbcnt_hi_u32_b32 v172, -1, v172
	v_lshrrev_b32_e32 v173, 3, v172
	v_and_b32_e32 v172, 7, v172
	v_lshlrev_b32_e32 v166, 16, v173
	v_lshl_add_u32 v166, v172, 4, v166
	v_add_u32_e32 v167, 0x1000, v166
	v_add_u32_e32 v168, 0x2000, v166
	v_add_u32_e32 v169, 0x3000, v166
	v_lshlrev_b32_e32 v170, 12, v172
	v_lshl_add_u32 v170, v173, 4, v170
	v_mov_b32_e32 v171, 0x43e00000
	s_mov_b32 s28, 0xc3e00000
	s_waitcnt lgkmcnt(0)
	s_add_u32 s10, s10, 0x2900000
	s_addc_u32 s11, s11, 0
	s_lshr_b32 s22, s4, 8
	s_and_b32 s23, s4, 0xff
	s_and_b32 s27, s22, 1
	s_lshr_b32 s22, s22, 1
	s_cmp_eq_u32 s27, 0
	s_cselect_b64 s[16:17], s[12:13], s[14:15]
	s_add_i32 s22, s22, 2
	s_lshl_b32 s24, s22, 22
	s_lshr_b32 s25, s23, 5
	s_lshl_b32 s25, s25, 19
	s_and_b32 s26, s23, 31
	s_lshl_b32 s26, s26, 7
	s_add_i32 s24, s24, s25
	s_add_i32 s24, s24, s26
	s_add_u32 s16, s16, s24
	s_addc_u32 s17, s17, 0
	s_nop 0
	global_load_dwordx4 v[0:3], v166, s[16:17] nt
	global_load_dwordx4 v[4:7], v167, s[16:17] nt
	global_load_dwordx4 v[8:11], v168, s[16:17] nt
	global_load_dwordx4 v[12:15], v169, s[16:17] nt
	s_add_u32 s16, s16, 0x4000
	s_addc_u32 s17, s17, 0
	s_nop 0
	global_load_dwordx4 v[16:19], v166, s[16:17] nt
	global_load_dwordx4 v[20:23], v167, s[16:17] nt
	global_load_dwordx4 v[24:27], v168, s[16:17] nt
	global_load_dwordx4 v[28:31], v169, s[16:17] nt
	s_add_u32 s16, s16, 0x4000
	s_addc_u32 s17, s17, 0
	s_nop 0
	global_load_dwordx4 v[32:35], v166, s[16:17] nt
	global_load_dwordx4 v[36:39], v167, s[16:17] nt
	global_load_dwordx4 v[40:43], v168, s[16:17] nt
	global_load_dwordx4 v[44:47], v169, s[16:17] nt
	s_add_u32 s16, s16, 0x4000
	s_addc_u32 s17, s17, 0
	s_nop 0
	global_load_dwordx4 v[48:51], v166, s[16:17] nt
	global_load_dwordx4 v[52:55], v167, s[16:17] nt
	global_load_dwordx4 v[56:59], v168, s[16:17] nt
	global_load_dwordx4 v[60:63], v169, s[16:17] nt
	s_add_i32 s7, s4, s5
	s_cmp_lt_u32 s7, s6
	s_cbranch_scc0 .Lp4c0_p_last
	s_lshr_b32 s22, s7, 8
	s_and_b32 s23, s7, 0xff
	s_and_b32 s27, s22, 1
	s_lshr_b32 s22, s22, 1
	s_cmp_eq_u32 s27, 0
	s_cselect_b64 s[16:17], s[12:13], s[14:15]
	s_add_i32 s22, s22, 2
	s_lshl_b32 s24, s22, 22
	s_lshr_b32 s25, s23, 5
	s_lshl_b32 s25, s25, 19
	s_and_b32 s26, s23, 31
	s_lshl_b32 s26, s26, 7
	s_add_i32 s24, s24, s25
	s_add_i32 s24, s24, s26
	s_add_u32 s16, s16, s24
	s_addc_u32 s17, s17, 0
	s_nop 0
	global_load_dwordx4 v[64:67], v166, s[16:17] nt
	global_load_dwordx4 v[68:71], v167, s[16:17] nt
	global_load_dwordx4 v[72:75], v168, s[16:17] nt
	global_load_dwordx4 v[76:79], v169, s[16:17] nt
	s_add_u32 s16, s16, 0x4000
	s_addc_u32 s17, s17, 0
	s_nop 0
	global_load_dwordx4 v[80:83], v166, s[16:17] nt
	global_load_dwordx4 v[84:87], v167, s[16:17] nt
	global_load_dwordx4 v[88:91], v168, s[16:17] nt
	global_load_dwordx4 v[92:95], v169, s[16:17] nt
	s_add_u32 s16, s16, 0x4000
	s_addc_u32 s17, s17, 0
	s_nop 0
	global_load_dwordx4 v[96:99], v166, s[16:17] nt
	global_load_dwordx4 v[100:103], v167, s[16:17] nt
	global_load_dwordx4 v[104:107], v168, s[16:17] nt
	global_load_dwordx4 v[108:111], v169, s[16:17] nt
	s_add_u32 s16, s16, 0x4000
	s_addc_u32 s17, s17, 0
	s_nop 0
	global_load_dwordx4 v[112:115], v166, s[16:17] nt
	global_load_dwordx4 v[116:119], v167, s[16:17] nt
	global_load_dwordx4 v[120:123], v168, s[16:17] nt
	global_load_dwordx4 v[124:127], v169, s[16:17] nt
	s_waitcnt vmcnt(16)
	s_branch .Lp4c0_p_st

.Lp4c0_p_st:
	s_lshr_b32 s22, s4, 8
	s_and_b32 s23, s4, 0xff
	s_and_b32 s27, s22, 1
	s_lshr_b32 s22, s22, 1
	s_add_i32 s22, s22, 2
	s_mul_i32 s24, s22, 0x300000
	s_lshr_b32 s25, s23, 5
	s_lshl_b32 s25, s25, 7
	s_add_i32 s24, s24, s25
	s_and_b32 s26, s23, 31
	s_lshr_b32 s25, s26, 2
	s_lshl_b32 s25, s25, 18
	s_add_i32 s24, s24, s25
	s_lshl_b32 s25, s27, 17
	s_add_i32 s24, s24, s25
	s_and_b32 s25, s26, 3
	s_lshl_b32 s25, s25, 15
	s_add_i32 s24, s24, s25
	s_add_u32 s20, s10, s24
	s_addc_u32 s21, s11, 0
	v_mul_f32_e32 v0, 0x42000000, v0
	v_mul_f32_e32 v4, 0x42000000, v4
	v_mul_f32_e32 v8, 0x42000000, v8
	v_mul_f32_e32 v12, 0x42000000, v12
	v_mul_f32_e32 v16, 0x42000000, v16
	v_mul_f32_e32 v20, 0x42000000, v20
	v_mul_f32_e32 v24, 0x42000000, v24
	v_mul_f32_e32 v28, 0x42000000, v28
	v_mul_f32_e32 v32, 0x42000000, v32
	v_mul_f32_e32 v36, 0x42000000, v36
	v_mul_f32_e32 v40, 0x42000000, v40
	v_mul_f32_e32 v44, 0x42000000, v44
	v_mul_f32_e32 v48, 0x42000000, v48
	v_mul_f32_e32 v52, 0x42000000, v52
	v_mul_f32_e32 v56, 0x42000000, v56
	v_mul_f32_e32 v60, 0x42000000, v60
	v_med3_f32 v0, v0, s28, v171
	v_med3_f32 v4, v4, s28, v171
	v_med3_f32 v8, v8, s28, v171
	v_med3_f32 v12, v12, s28, v171
	v_med3_f32 v16, v16, s28, v171
	v_med3_f32 v20, v20, s28, v171
	v_med3_f32 v24, v24, s28, v171
	v_med3_f32 v28, v28, s28, v171
	v_med3_f32 v32, v32, s28, v171
	v_med3_f32 v36, v36, s28, v171
	v_med3_f32 v40, v40, s28, v171
	v_med3_f32 v44, v44, s28, v171
	v_med3_f32 v48, v48, s28, v171
	v_med3_f32 v52, v52, s28, v171
	v_med3_f32 v56, v56, s28, v171
	v_med3_f32 v60, v60, s28, v171
	v_cvt_pk_fp8_f32 v158, v0, v4
	v_cvt_pk_fp8_f32 v159, v16, v20
	v_cvt_pk_fp8_f32 v160, v32, v36
	v_cvt_pk_fp8_f32 v161, v48, v52
	v_cvt_pk_fp8_f32 v158, v8, v12 op_sel:[0,0,1]
	v_cvt_pk_fp8_f32 v159, v24, v28 op_sel:[0,0,1]
	v_cvt_pk_fp8_f32 v160, v40, v44 op_sel:[0,0,1]
	v_cvt_pk_fp8_f32 v161, v56, v60 op_sel:[0,0,1]
	s_nop 0
	global_store_dwordx4 v170, v[158:161], s[20:21]
	v_mul_f32_e32 v1, 0x42000000, v1
	v_mul_f32_e32 v5, 0x42000000, v5
	v_mul_f32_e32 v9, 0x42000000, v9
	v_mul_f32_e32 v13, 0x42000000, v13
	v_mul_f32_e32 v17, 0x42000000, v17
	v_mul_f32_e32 v21, 0x42000000, v21
	v_mul_f32_e32 v25, 0x42000000, v25
	v_mul_f32_e32 v29, 0x42000000, v29
	v_mul_f32_e32 v33, 0x42000000, v33
	v_mul_f32_e32 v37, 0x42000000, v37
	v_mul_f32_e32 v41, 0x42000000, v41
	v_mul_f32_e32 v45, 0x42000000, v45
	v_mul_f32_e32 v49, 0x42000000, v49
	v_mul_f32_e32 v53, 0x42000000, v53
	v_mul_f32_e32 v57, 0x42000000, v57
	v_mul_f32_e32 v61, 0x42000000, v61
	v_med3_f32 v1, v1, s28, v171
	v_med3_f32 v5, v5, s28, v171
	v_med3_f32 v9, v9, s28, v171
	v_med3_f32 v13, v13, s28, v171
	v_med3_f32 v17, v17, s28, v171
	v_med3_f32 v21, v21, s28, v171
	v_med3_f32 v25, v25, s28, v171
	v_med3_f32 v29, v29, s28, v171
	v_med3_f32 v33, v33, s28, v171
	v_med3_f32 v37, v37, s28, v171
	v_med3_f32 v41, v41, s28, v171
	v_med3_f32 v45, v45, s28, v171
	v_med3_f32 v49, v49, s28, v171
	v_med3_f32 v53, v53, s28, v171
	v_med3_f32 v57, v57, s28, v171
	v_med3_f32 v61, v61, s28, v171
	v_cvt_pk_fp8_f32 v162, v1, v5
	v_cvt_pk_fp8_f32 v163, v17, v21
	v_cvt_pk_fp8_f32 v164, v33, v37
	v_cvt_pk_fp8_f32 v165, v49, v53
	v_cvt_pk_fp8_f32 v162, v9, v13 op_sel:[0,0,1]
	v_cvt_pk_fp8_f32 v163, v25, v29 op_sel:[0,0,1]
	v_cvt_pk_fp8_f32 v164, v41, v45 op_sel:[0,0,1]
	v_cvt_pk_fp8_f32 v165, v57, v61 op_sel:[0,0,1]
	s_nop 0
	global_store_dwordx4 v170, v[162:165], s[20:21] offset:1024
	v_mul_f32_e32 v2, 0x42000000, v2
	v_mul_f32_e32 v6, 0x42000000, v6
	v_mul_f32_e32 v10, 0x42000000, v10
	v_mul_f32_e32 v14, 0x42000000, v14
	v_mul_f32_e32 v18, 0x42000000, v18
	v_mul_f32_e32 v22, 0x42000000, v22
	v_mul_f32_e32 v26, 0x42000000, v26
	v_mul_f32_e32 v30, 0x42000000, v30
	v_mul_f32_e32 v34, 0x42000000, v34
	v_mul_f32_e32 v38, 0x42000000, v38
	v_mul_f32_e32 v42, 0x42000000, v42
	v_mul_f32_e32 v46, 0x42000000, v46
	v_mul_f32_e32 v50, 0x42000000, v50
	v_mul_f32_e32 v54, 0x42000000, v54
	v_mul_f32_e32 v58, 0x42000000, v58
	v_mul_f32_e32 v62, 0x42000000, v62
	v_med3_f32 v2, v2, s28, v171
	v_med3_f32 v6, v6, s28, v171
	v_med3_f32 v10, v10, s28, v171
	v_med3_f32 v14, v14, s28, v171
	v_med3_f32 v18, v18, s28, v171
	v_med3_f32 v22, v22, s28, v171
	v_med3_f32 v26, v26, s28, v171
	v_med3_f32 v30, v30, s28, v171
	v_med3_f32 v34, v34, s28, v171
	v_med3_f32 v38, v38, s28, v171
	v_med3_f32 v42, v42, s28, v171
	v_med3_f32 v46, v46, s28, v171
	v_med3_f32 v50, v50, s28, v171
	v_med3_f32 v54, v54, s28, v171
	v_med3_f32 v58, v58, s28, v171
	v_med3_f32 v62, v62, s28, v171
	v_cvt_pk_fp8_f32 v158, v2, v6
	v_cvt_pk_fp8_f32 v159, v18, v22
	v_cvt_pk_fp8_f32 v160, v34, v38
	v_cvt_pk_fp8_f32 v161, v50, v54
	v_cvt_pk_fp8_f32 v158, v10, v14 op_sel:[0,0,1]
	v_cvt_pk_fp8_f32 v159, v26, v30 op_sel:[0,0,1]
	v_cvt_pk_fp8_f32 v160, v42, v46 op_sel:[0,0,1]
	v_cvt_pk_fp8_f32 v161, v58, v62 op_sel:[0,0,1]
	s_nop 0
	global_store_dwordx4 v170, v[158:161], s[20:21] offset:2048
	v_mul_f32_e32 v3, 0x42000000, v3
	v_mul_f32_e32 v7, 0x42000000, v7
	v_mul_f32_e32 v11, 0x42000000, v11
	v_mul_f32_e32 v15, 0x42000000, v15
	v_mul_f32_e32 v19, 0x42000000, v19
	v_mul_f32_e32 v23, 0x42000000, v23
	v_mul_f32_e32 v27, 0x42000000, v27
	v_mul_f32_e32 v31, 0x42000000, v31
	v_mul_f32_e32 v35, 0x42000000, v35
	v_mul_f32_e32 v39, 0x42000000, v39
	v_mul_f32_e32 v43, 0x42000000, v43
	v_mul_f32_e32 v47, 0x42000000, v47
	v_mul_f32_e32 v51, 0x42000000, v51
	v_mul_f32_e32 v55, 0x42000000, v55
	v_mul_f32_e32 v59, 0x42000000, v59
	v_mul_f32_e32 v63, 0x42000000, v63
	v_med3_f32 v3, v3, s28, v171
	v_med3_f32 v7, v7, s28, v171
	v_med3_f32 v11, v11, s28, v171
	v_med3_f32 v15, v15, s28, v171
	v_med3_f32 v19, v19, s28, v171
	v_med3_f32 v23, v23, s28, v171
	v_med3_f32 v27, v27, s28, v171
	v_med3_f32 v31, v31, s28, v171
	v_med3_f32 v35, v35, s28, v171
	v_med3_f32 v39, v39, s28, v171
	v_med3_f32 v43, v43, s28, v171
	v_med3_f32 v47, v47, s28, v171
	v_med3_f32 v51, v51, s28, v171
	v_med3_f32 v55, v55, s28, v171
	v_med3_f32 v59, v59, s28, v171
	v_med3_f32 v63, v63, s28, v171
	v_cvt_pk_fp8_f32 v162, v3, v7
	v_cvt_pk_fp8_f32 v163, v19, v23
	v_cvt_pk_fp8_f32 v164, v35, v39
	v_cvt_pk_fp8_f32 v165, v51, v55
	v_cvt_pk_fp8_f32 v162, v11, v15 op_sel:[0,0,1]
	v_cvt_pk_fp8_f32 v163, v27, v31 op_sel:[0,0,1]
	v_cvt_pk_fp8_f32 v164, v43, v47 op_sel:[0,0,1]
	v_cvt_pk_fp8_f32 v165, v59, v63 op_sel:[0,0,1]
	s_nop 0
	global_store_dwordx4 v170, v[162:165], s[20:21] offset:3072
	s_cmp_ge_u32 s7, s6
	s_cbranch_scc1 .Lp4c0_done
	s_mov_b32 s4, s7
.Lp4c0_loop:
	s_add_i32 s7, s4, s5
	s_cmp_lt_u32 s7, s6
	s_cbranch_scc0 .Lp4c0_B_last
	s_lshr_b32 s22, s7, 8
	s_and_b32 s23, s7, 0xff
	s_and_b32 s27, s22, 1
	s_lshr_b32 s22, s22, 1
	s_cmp_eq_u32 s27, 0
	s_cselect_b64 s[16:17], s[12:13], s[14:15]
	s_add_i32 s22, s22, 2
	s_lshl_b32 s24, s22, 22
	s_lshr_b32 s25, s23, 5
	s_lshl_b32 s25, s25, 19
	s_and_b32 s26, s23, 31
	s_lshl_b32 s26, s26, 7
	s_add_i32 s24, s24, s25
	s_add_i32 s24, s24, s26
	s_add_u32 s16, s16, s24
	s_addc_u32 s17, s17, 0
	s_nop 0
	global_load_dwordx4 v[0:3], v166, s[16:17] nt
	global_load_dwordx4 v[4:7], v167, s[16:17] nt
	global_load_dwordx4 v[8:11], v168, s[16:17] nt
	global_load_dwordx4 v[12:15], v169, s[16:17] nt
	s_add_u32 s16, s16, 0x4000
	s_addc_u32 s17, s17, 0
	s_nop 0
	global_load_dwordx4 v[16:19], v166, s[16:17] nt
	global_load_dwordx4 v[20:23], v167, s[16:17] nt
	global_load_dwordx4 v[24:27], v168, s[16:17] nt
	global_load_dwordx4 v[28:31], v169, s[16:17] nt
	s_add_u32 s16, s16, 0x4000
	s_addc_u32 s17, s17, 0
	s_nop 0
	global_load_dwordx4 v[32:35], v166, s[16:17] nt
	global_load_dwordx4 v[36:39], v167, s[16:17] nt
	global_load_dwordx4 v[40:43], v168, s[16:17] nt
	global_load_dwordx4 v[44:47], v169, s[16:17] nt
	s_add_u32 s16, s16, 0x4000
	s_addc_u32 s17, s17, 0
	s_nop 0
	global_load_dwordx4 v[48:51], v166, s[16:17] nt
	global_load_dwordx4 v[52:55], v167, s[16:17] nt
	global_load_dwordx4 v[56:59], v168, s[16:17] nt
	global_load_dwordx4 v[60:63], v169, s[16:17] nt
	s_waitcnt vmcnt(20)
	s_branch .Lp4c0_B_st

.Lp4c0_B_st:
	s_lshr_b32 s22, s4, 8
	s_and_b32 s23, s4, 0xff
	s_and_b32 s27, s22, 1
	s_lshr_b32 s22, s22, 1
	s_add_i32 s22, s22, 2
	s_mul_i32 s24, s22, 0x300000
	s_lshr_b32 s25, s23, 5
	s_lshl_b32 s25, s25, 7
	s_add_i32 s24, s24, s25
	s_and_b32 s26, s23, 31
	s_lshr_b32 s25, s26, 2
	s_lshl_b32 s25, s25, 18
	s_add_i32 s24, s24, s25
	s_lshl_b32 s25, s27, 17
	s_add_i32 s24, s24, s25
	s_and_b32 s25, s26, 3
	s_lshl_b32 s25, s25, 15
	s_add_i32 s24, s24, s25
	s_add_u32 s20, s10, s24
	s_addc_u32 s21, s11, 0
	v_mul_f32_e32 v64, 0x42000000, v64
	v_mul_f32_e32 v68, 0x42000000, v68
	v_mul_f32_e32 v72, 0x42000000, v72
	v_mul_f32_e32 v76, 0x42000000, v76
	v_mul_f32_e32 v80, 0x42000000, v80
	v_mul_f32_e32 v84, 0x42000000, v84
	v_mul_f32_e32 v88, 0x42000000, v88
	v_mul_f32_e32 v92, 0x42000000, v92
	v_mul_f32_e32 v96, 0x42000000, v96
	v_mul_f32_e32 v100, 0x42000000, v100
	v_mul_f32_e32 v104, 0x42000000, v104
	v_mul_f32_e32 v108, 0x42000000, v108
	v_mul_f32_e32 v112, 0x42000000, v112
	v_mul_f32_e32 v116, 0x42000000, v116
	v_mul_f32_e32 v120, 0x42000000, v120
	v_mul_f32_e32 v124, 0x42000000, v124
	v_med3_f32 v64, v64, s28, v171
	v_med3_f32 v68, v68, s28, v171
	v_med3_f32 v72, v72, s28, v171
	v_med3_f32 v76, v76, s28, v171
	v_med3_f32 v80, v80, s28, v171
	v_med3_f32 v84, v84, s28, v171
	v_med3_f32 v88, v88, s28, v171
	v_med3_f32 v92, v92, s28, v171
	v_med3_f32 v96, v96, s28, v171
	v_med3_f32 v100, v100, s28, v171
	v_med3_f32 v104, v104, s28, v171
	v_med3_f32 v108, v108, s28, v171
	v_med3_f32 v112, v112, s28, v171
	v_med3_f32 v116, v116, s28, v171
	v_med3_f32 v120, v120, s28, v171
	v_med3_f32 v124, v124, s28, v171
	v_cvt_pk_fp8_f32 v158, v64, v68
	v_cvt_pk_fp8_f32 v159, v80, v84
	v_cvt_pk_fp8_f32 v160, v96, v100
	v_cvt_pk_fp8_f32 v161, v112, v116
	v_cvt_pk_fp8_f32 v158, v72, v76 op_sel:[0,0,1]
	v_cvt_pk_fp8_f32 v159, v88, v92 op_sel:[0,0,1]
	v_cvt_pk_fp8_f32 v160, v104, v108 op_sel:[0,0,1]
	v_cvt_pk_fp8_f32 v161, v120, v124 op_sel:[0,0,1]
	s_nop 0
	global_store_dwordx4 v170, v[158:161], s[20:21]
	v_mul_f32_e32 v65, 0x42000000, v65
	v_mul_f32_e32 v69, 0x42000000, v69
	v_mul_f32_e32 v73, 0x42000000, v73
	v_mul_f32_e32 v77, 0x42000000, v77
	v_mul_f32_e32 v81, 0x42000000, v81
	v_mul_f32_e32 v85, 0x42000000, v85
	v_mul_f32_e32 v89, 0x42000000, v89
	v_mul_f32_e32 v93, 0x42000000, v93
	v_mul_f32_e32 v97, 0x42000000, v97
	v_mul_f32_e32 v101, 0x42000000, v101
	v_mul_f32_e32 v105, 0x42000000, v105
	v_mul_f32_e32 v109, 0x42000000, v109
	v_mul_f32_e32 v113, 0x42000000, v113
	v_mul_f32_e32 v117, 0x42000000, v117
	v_mul_f32_e32 v121, 0x42000000, v121
	v_mul_f32_e32 v125, 0x42000000, v125
	v_med3_f32 v65, v65, s28, v171
	v_med3_f32 v69, v69, s28, v171
	v_med3_f32 v73, v73, s28, v171
	v_med3_f32 v77, v77, s28, v171
	v_med3_f32 v81, v81, s28, v171
	v_med3_f32 v85, v85, s28, v171
	v_med3_f32 v89, v89, s28, v171
	v_med3_f32 v93, v93, s28, v171
	v_med3_f32 v97, v97, s28, v171
	v_med3_f32 v101, v101, s28, v171
	v_med3_f32 v105, v105, s28, v171
	v_med3_f32 v109, v109, s28, v171
	v_med3_f32 v113, v113, s28, v171
	v_med3_f32 v117, v117, s28, v171
	v_med3_f32 v121, v121, s28, v171
	v_med3_f32 v125, v125, s28, v171
	v_cvt_pk_fp8_f32 v162, v65, v69
	v_cvt_pk_fp8_f32 v163, v81, v85
	v_cvt_pk_fp8_f32 v164, v97, v101
	v_cvt_pk_fp8_f32 v165, v113, v117
	v_cvt_pk_fp8_f32 v162, v73, v77 op_sel:[0,0,1]
	v_cvt_pk_fp8_f32 v163, v89, v93 op_sel:[0,0,1]
	v_cvt_pk_fp8_f32 v164, v105, v109 op_sel:[0,0,1]
	v_cvt_pk_fp8_f32 v165, v121, v125 op_sel:[0,0,1]
	s_nop 0
	global_store_dwordx4 v170, v[162:165], s[20:21] offset:1024
	v_mul_f32_e32 v66, 0x42000000, v66
	v_mul_f32_e32 v70, 0x42000000, v70
	v_mul_f32_e32 v74, 0x42000000, v74
	v_mul_f32_e32 v78, 0x42000000, v78
	v_mul_f32_e32 v82, 0x42000000, v82
	v_mul_f32_e32 v86, 0x42000000, v86
	v_mul_f32_e32 v90, 0x42000000, v90
	v_mul_f32_e32 v94, 0x42000000, v94
	v_mul_f32_e32 v98, 0x42000000, v98
	v_mul_f32_e32 v102, 0x42000000, v102
	v_mul_f32_e32 v106, 0x42000000, v106
	v_mul_f32_e32 v110, 0x42000000, v110
	v_mul_f32_e32 v114, 0x42000000, v114
	v_mul_f32_e32 v118, 0x42000000, v118
	v_mul_f32_e32 v122, 0x42000000, v122
	v_mul_f32_e32 v126, 0x42000000, v126
	v_med3_f32 v66, v66, s28, v171
	v_med3_f32 v70, v70, s28, v171
	v_med3_f32 v74, v74, s28, v171
	v_med3_f32 v78, v78, s28, v171
	v_med3_f32 v82, v82, s28, v171
	v_med3_f32 v86, v86, s28, v171
	v_med3_f32 v90, v90, s28, v171
	v_med3_f32 v94, v94, s28, v171
	v_med3_f32 v98, v98, s28, v171
	v_med3_f32 v102, v102, s28, v171
	v_med3_f32 v106, v106, s28, v171
	v_med3_f32 v110, v110, s28, v171
	v_med3_f32 v114, v114, s28, v171
	v_med3_f32 v118, v118, s28, v171
	v_med3_f32 v122, v122, s28, v171
	v_med3_f32 v126, v126, s28, v171
	v_cvt_pk_fp8_f32 v158, v66, v70
	v_cvt_pk_fp8_f32 v159, v82, v86
	v_cvt_pk_fp8_f32 v160, v98, v102
	v_cvt_pk_fp8_f32 v161, v114, v118
	v_cvt_pk_fp8_f32 v158, v74, v78 op_sel:[0,0,1]
	v_cvt_pk_fp8_f32 v159, v90, v94 op_sel:[0,0,1]
	v_cvt_pk_fp8_f32 v160, v106, v110 op_sel:[0,0,1]
	v_cvt_pk_fp8_f32 v161, v122, v126 op_sel:[0,0,1]
	s_nop 0
	global_store_dwordx4 v170, v[158:161], s[20:21] offset:2048
	v_mul_f32_e32 v67, 0x42000000, v67
	v_mul_f32_e32 v71, 0x42000000, v71
	v_mul_f32_e32 v75, 0x42000000, v75
	v_mul_f32_e32 v79, 0x42000000, v79
	v_mul_f32_e32 v83, 0x42000000, v83
	v_mul_f32_e32 v87, 0x42000000, v87
	v_mul_f32_e32 v91, 0x42000000, v91
	v_mul_f32_e32 v95, 0x42000000, v95
	v_mul_f32_e32 v99, 0x42000000, v99
	v_mul_f32_e32 v103, 0x42000000, v103
	v_mul_f32_e32 v107, 0x42000000, v107
	v_mul_f32_e32 v111, 0x42000000, v111
	v_mul_f32_e32 v115, 0x42000000, v115
	v_mul_f32_e32 v119, 0x42000000, v119
	v_mul_f32_e32 v123, 0x42000000, v123
	v_mul_f32_e32 v127, 0x42000000, v127
	v_med3_f32 v67, v67, s28, v171
	v_med3_f32 v71, v71, s28, v171
	v_med3_f32 v75, v75, s28, v171
	v_med3_f32 v79, v79, s28, v171
	v_med3_f32 v83, v83, s28, v171
	v_med3_f32 v87, v87, s28, v171
	v_med3_f32 v91, v91, s28, v171
	v_med3_f32 v95, v95, s28, v171
	v_med3_f32 v99, v99, s28, v171
	v_med3_f32 v103, v103, s28, v171
	v_med3_f32 v107, v107, s28, v171
	v_med3_f32 v111, v111, s28, v171
	v_med3_f32 v115, v115, s28, v171
	v_med3_f32 v119, v119, s28, v171
	v_med3_f32 v123, v123, s28, v171
	v_med3_f32 v127, v127, s28, v171
	v_cvt_pk_fp8_f32 v162, v67, v71
	v_cvt_pk_fp8_f32 v163, v83, v87
	v_cvt_pk_fp8_f32 v164, v99, v103
	v_cvt_pk_fp8_f32 v165, v115, v119
	v_cvt_pk_fp8_f32 v162, v75, v79 op_sel:[0,0,1]
	v_cvt_pk_fp8_f32 v163, v91, v95 op_sel:[0,0,1]
	v_cvt_pk_fp8_f32 v164, v107, v111 op_sel:[0,0,1]
	v_cvt_pk_fp8_f32 v165, v123, v127 op_sel:[0,0,1]
	s_nop 0
	global_store_dwordx4 v170, v[162:165], s[20:21] offset:3072
	s_cmp_ge_u32 s7, s6
	s_cbranch_scc1 .Lp4c0_done
	s_mov_b32 s4, s7
	s_add_i32 s7, s4, s5
	s_cmp_lt_u32 s7, s6
	s_cbranch_scc0 .Lp4c0_A_last
	s_lshr_b32 s22, s7, 8
	s_and_b32 s23, s7, 0xff
	s_and_b32 s27, s22, 1
	s_lshr_b32 s22, s22, 1
	s_cmp_eq_u32 s27, 0
	s_cselect_b64 s[16:17], s[12:13], s[14:15]
	s_add_i32 s22, s22, 2
	s_lshl_b32 s24, s22, 22
	s_lshr_b32 s25, s23, 5
	s_lshl_b32 s25, s25, 19
	s_and_b32 s26, s23, 31
	s_lshl_b32 s26, s26, 7
	s_add_i32 s24, s24, s25
	s_add_i32 s24, s24, s26
	s_add_u32 s16, s16, s24
	s_addc_u32 s17, s17, 0
	s_nop 0
	global_load_dwordx4 v[64:67], v166, s[16:17] nt
	global_load_dwordx4 v[68:71], v167, s[16:17] nt
	global_load_dwordx4 v[72:75], v168, s[16:17] nt
	global_load_dwordx4 v[76:79], v169, s[16:17] nt
	s_add_u32 s16, s16, 0x4000
	s_addc_u32 s17, s17, 0
	s_nop 0
	global_load_dwordx4 v[80:83], v166, s[16:17] nt
	global_load_dwordx4 v[84:87], v167, s[16:17] nt
	global_load_dwordx4 v[88:91], v168, s[16:17] nt
	global_load_dwordx4 v[92:95], v169, s[16:17] nt
	s_add_u32 s16, s16, 0x4000
	s_addc_u32 s17, s17, 0
	s_nop 0
	global_load_dwordx4 v[96:99], v166, s[16:17] nt
	global_load_dwordx4 v[100:103], v167, s[16:17] nt
	global_load_dwordx4 v[104:107], v168, s[16:17] nt
	global_load_dwordx4 v[108:111], v169, s[16:17] nt
	s_add_u32 s16, s16, 0x4000
	s_addc_u32 s17, s17, 0
	s_nop 0
	global_load_dwordx4 v[112:115], v166, s[16:17] nt
	global_load_dwordx4 v[116:119], v167, s[16:17] nt
	global_load_dwordx4 v[120:123], v168, s[16:17] nt
	global_load_dwordx4 v[124:127], v169, s[16:17] nt
	s_waitcnt vmcnt(20)
	s_branch .Lp4c0_A_st

.Lp4c0_A_st:
	s_lshr_b32 s22, s4, 8
	s_and_b32 s23, s4, 0xff
	s_and_b32 s27, s22, 1
	s_lshr_b32 s22, s22, 1
	s_add_i32 s22, s22, 2
	s_mul_i32 s24, s22, 0x300000
	s_lshr_b32 s25, s23, 5
	s_lshl_b32 s25, s25, 7
	s_add_i32 s24, s24, s25
	s_and_b32 s26, s23, 31
	s_lshr_b32 s25, s26, 2
	s_lshl_b32 s25, s25, 18
	s_add_i32 s24, s24, s25
	s_lshl_b32 s25, s27, 17
	s_add_i32 s24, s24, s25
	s_and_b32 s25, s26, 3
	s_lshl_b32 s25, s25, 15
	s_add_i32 s24, s24, s25
	s_add_u32 s20, s10, s24
	s_addc_u32 s21, s11, 0
	v_mul_f32_e32 v0, 0x42000000, v0
	v_mul_f32_e32 v4, 0x42000000, v4
	v_mul_f32_e32 v8, 0x42000000, v8
	v_mul_f32_e32 v12, 0x42000000, v12
	v_mul_f32_e32 v16, 0x42000000, v16
	v_mul_f32_e32 v20, 0x42000000, v20
	v_mul_f32_e32 v24, 0x42000000, v24
	v_mul_f32_e32 v28, 0x42000000, v28
	v_mul_f32_e32 v32, 0x42000000, v32
	v_mul_f32_e32 v36, 0x42000000, v36
	v_mul_f32_e32 v40, 0x42000000, v40
	v_mul_f32_e32 v44, 0x42000000, v44
	v_mul_f32_e32 v48, 0x42000000, v48
	v_mul_f32_e32 v52, 0x42000000, v52
	v_mul_f32_e32 v56, 0x42000000, v56
	v_mul_f32_e32 v60, 0x42000000, v60
	v_med3_f32 v0, v0, s28, v171
	v_med3_f32 v4, v4, s28, v171
	v_med3_f32 v8, v8, s28, v171
	v_med3_f32 v12, v12, s28, v171
	v_med3_f32 v16, v16, s28, v171
	v_med3_f32 v20, v20, s28, v171
	v_med3_f32 v24, v24, s28, v171
	v_med3_f32 v28, v28, s28, v171
	v_med3_f32 v32, v32, s28, v171
	v_med3_f32 v36, v36, s28, v171
	v_med3_f32 v40, v40, s28, v171
	v_med3_f32 v44, v44, s28, v171
	v_med3_f32 v48, v48, s28, v171
	v_med3_f32 v52, v52, s28, v171
	v_med3_f32 v56, v56, s28, v171
	v_med3_f32 v60, v60, s28, v171
	v_cvt_pk_fp8_f32 v158, v0, v4
	v_cvt_pk_fp8_f32 v159, v16, v20
	v_cvt_pk_fp8_f32 v160, v32, v36
	v_cvt_pk_fp8_f32 v161, v48, v52
	v_cvt_pk_fp8_f32 v158, v8, v12 op_sel:[0,0,1]
	v_cvt_pk_fp8_f32 v159, v24, v28 op_sel:[0,0,1]
	v_cvt_pk_fp8_f32 v160, v40, v44 op_sel:[0,0,1]
	v_cvt_pk_fp8_f32 v161, v56, v60 op_sel:[0,0,1]
	s_nop 0
	global_store_dwordx4 v170, v[158:161], s[20:21]
	v_mul_f32_e32 v1, 0x42000000, v1
	v_mul_f32_e32 v5, 0x42000000, v5
	v_mul_f32_e32 v9, 0x42000000, v9
	v_mul_f32_e32 v13, 0x42000000, v13
	v_mul_f32_e32 v17, 0x42000000, v17
	v_mul_f32_e32 v21, 0x42000000, v21
	v_mul_f32_e32 v25, 0x42000000, v25
	v_mul_f32_e32 v29, 0x42000000, v29
	v_mul_f32_e32 v33, 0x42000000, v33
	v_mul_f32_e32 v37, 0x42000000, v37
	v_mul_f32_e32 v41, 0x42000000, v41
	v_mul_f32_e32 v45, 0x42000000, v45
	v_mul_f32_e32 v49, 0x42000000, v49
	v_mul_f32_e32 v53, 0x42000000, v53
	v_mul_f32_e32 v57, 0x42000000, v57
	v_mul_f32_e32 v61, 0x42000000, v61
	v_med3_f32 v1, v1, s28, v171
	v_med3_f32 v5, v5, s28, v171
	v_med3_f32 v9, v9, s28, v171
	v_med3_f32 v13, v13, s28, v171
	v_med3_f32 v17, v17, s28, v171
	v_med3_f32 v21, v21, s28, v171
	v_med3_f32 v25, v25, s28, v171
	v_med3_f32 v29, v29, s28, v171
	v_med3_f32 v33, v33, s28, v171
	v_med3_f32 v37, v37, s28, v171
	v_med3_f32 v41, v41, s28, v171
	v_med3_f32 v45, v45, s28, v171
	v_med3_f32 v49, v49, s28, v171
	v_med3_f32 v53, v53, s28, v171
	v_med3_f32 v57, v57, s28, v171
	v_med3_f32 v61, v61, s28, v171
	v_cvt_pk_fp8_f32 v162, v1, v5
	v_cvt_pk_fp8_f32 v163, v17, v21
	v_cvt_pk_fp8_f32 v164, v33, v37
	v_cvt_pk_fp8_f32 v165, v49, v53
	v_cvt_pk_fp8_f32 v162, v9, v13 op_sel:[0,0,1]
	v_cvt_pk_fp8_f32 v163, v25, v29 op_sel:[0,0,1]
	v_cvt_pk_fp8_f32 v164, v41, v45 op_sel:[0,0,1]
	v_cvt_pk_fp8_f32 v165, v57, v61 op_sel:[0,0,1]
	s_nop 0
	global_store_dwordx4 v170, v[162:165], s[20:21] offset:1024
	v_mul_f32_e32 v2, 0x42000000, v2
	v_mul_f32_e32 v6, 0x42000000, v6
	v_mul_f32_e32 v10, 0x42000000, v10
	v_mul_f32_e32 v14, 0x42000000, v14
	v_mul_f32_e32 v18, 0x42000000, v18
	v_mul_f32_e32 v22, 0x42000000, v22
	v_mul_f32_e32 v26, 0x42000000, v26
	v_mul_f32_e32 v30, 0x42000000, v30
	v_mul_f32_e32 v34, 0x42000000, v34
	v_mul_f32_e32 v38, 0x42000000, v38
	v_mul_f32_e32 v42, 0x42000000, v42
	v_mul_f32_e32 v46, 0x42000000, v46
	v_mul_f32_e32 v50, 0x42000000, v50
	v_mul_f32_e32 v54, 0x42000000, v54
	v_mul_f32_e32 v58, 0x42000000, v58
	v_mul_f32_e32 v62, 0x42000000, v62
	v_med3_f32 v2, v2, s28, v171
	v_med3_f32 v6, v6, s28, v171
	v_med3_f32 v10, v10, s28, v171
	v_med3_f32 v14, v14, s28, v171
	v_med3_f32 v18, v18, s28, v171
	v_med3_f32 v22, v22, s28, v171
	v_med3_f32 v26, v26, s28, v171
	v_med3_f32 v30, v30, s28, v171
	v_med3_f32 v34, v34, s28, v171
	v_med3_f32 v38, v38, s28, v171
	v_med3_f32 v42, v42, s28, v171
	v_med3_f32 v46, v46, s28, v171
	v_med3_f32 v50, v50, s28, v171
	v_med3_f32 v54, v54, s28, v171
	v_med3_f32 v58, v58, s28, v171
	v_med3_f32 v62, v62, s28, v171
	v_cvt_pk_fp8_f32 v158, v2, v6
	v_cvt_pk_fp8_f32 v159, v18, v22
	v_cvt_pk_fp8_f32 v160, v34, v38
	v_cvt_pk_fp8_f32 v161, v50, v54
	v_cvt_pk_fp8_f32 v158, v10, v14 op_sel:[0,0,1]
	v_cvt_pk_fp8_f32 v159, v26, v30 op_sel:[0,0,1]
	v_cvt_pk_fp8_f32 v160, v42, v46 op_sel:[0,0,1]
	v_cvt_pk_fp8_f32 v161, v58, v62 op_sel:[0,0,1]
	s_nop 0
	global_store_dwordx4 v170, v[158:161], s[20:21] offset:2048
	v_mul_f32_e32 v3, 0x42000000, v3
	v_mul_f32_e32 v7, 0x42000000, v7
	v_mul_f32_e32 v11, 0x42000000, v11
	v_mul_f32_e32 v15, 0x42000000, v15
	v_mul_f32_e32 v19, 0x42000000, v19
	v_mul_f32_e32 v23, 0x42000000, v23
	v_mul_f32_e32 v27, 0x42000000, v27
	v_mul_f32_e32 v31, 0x42000000, v31
	v_mul_f32_e32 v35, 0x42000000, v35
	v_mul_f32_e32 v39, 0x42000000, v39
	v_mul_f32_e32 v43, 0x42000000, v43
	v_mul_f32_e32 v47, 0x42000000, v47
	v_mul_f32_e32 v51, 0x42000000, v51
	v_mul_f32_e32 v55, 0x42000000, v55
	v_mul_f32_e32 v59, 0x42000000, v59
	v_mul_f32_e32 v63, 0x42000000, v63
	v_med3_f32 v3, v3, s28, v171
	v_med3_f32 v7, v7, s28, v171
	v_med3_f32 v11, v11, s28, v171
	v_med3_f32 v15, v15, s28, v171
	v_med3_f32 v19, v19, s28, v171
	v_med3_f32 v23, v23, s28, v171
	v_med3_f32 v27, v27, s28, v171
	v_med3_f32 v31, v31, s28, v171
	v_med3_f32 v35, v35, s28, v171
	v_med3_f32 v39, v39, s28, v171
	v_med3_f32 v43, v43, s28, v171
	v_med3_f32 v47, v47, s28, v171
	v_med3_f32 v51, v51, s28, v171
	v_med3_f32 v55, v55, s28, v171
	v_med3_f32 v59, v59, s28, v171
	v_med3_f32 v63, v63, s28, v171
	v_cvt_pk_fp8_f32 v162, v3, v7
	v_cvt_pk_fp8_f32 v163, v19, v23
	v_cvt_pk_fp8_f32 v164, v35, v39
	v_cvt_pk_fp8_f32 v165, v51, v55
	v_cvt_pk_fp8_f32 v162, v11, v15 op_sel:[0,0,1]
	v_cvt_pk_fp8_f32 v163, v27, v31 op_sel:[0,0,1]
	v_cvt_pk_fp8_f32 v164, v43, v47 op_sel:[0,0,1]
	v_cvt_pk_fp8_f32 v165, v59, v63 op_sel:[0,0,1]
	s_nop 0
	global_store_dwordx4 v170, v[162:165], s[20:21] offset:3072
	s_cmp_ge_u32 s7, s6
	s_cbranch_scc1 .Lp4c0_done
	s_mov_b32 s4, s7
	s_branch .Lp4c0_loop
.Lp4c0_done:
	s_mov_b64 s[4:5], s[30:31]

.LBB0_740:
	s_load_dwordx4 s[0:3], s[8:9], 0x138
	s_waitcnt lgkmcnt(0)
	s_mov_b64 s[4:5], s[0:1]
	s_cmp_lt_i32 s4, 7
	s_cselect_b64 s[0:1], -1, 0
	s_cmp_gt_i32 s5, 6
	s_cselect_b64 s[2:3], -1, 0
	s_and_b64 s[0:1], s[0:1], s[2:3]
	s_andn2_b64 vcc, exec, s[0:1]
	s_cbranch_vccnz .LBB0_960
	s_mov_b64 s[0:1], s[8:9]
	v_mbcnt_lo_u32_b32 v135, -1, 0
	v_mbcnt_hi_u32_b32 v135, -1, v135
	s_load_dword s74, s[8:9], 0x148
	s_add_u32 s2, s8, 0x148
	v_readlane_b32 s4, v243, 0
	s_addc_u32 s3, s9, 0
	v_readlane_b32 s5, v243, 1
	s_waitcnt lgkmcnt(0)
	s_sub_i32 s18, s74, 32
	s_cmp_lt_i32 s4, s18
	s_mov_b64 s[4:5], -1
	s_cbranch_scc1 .LBB0_777
	v_readlane_b32 s4, v243, 0
	s_sub_i32 s4, s4, s18
	s_lshl_b32 s4, s4, 3
	s_add_i32 s19, s4, s94
	s_mov_b32 s4, s19
	s_mov_b32 s5, 0x100
	s_mov_b32 s6, 0x4000
	s_waitcnt vmcnt(0)
	s_cmp_ge_u32 s4, s6
	s_cbranch_scc1 .Lp6c0_done
	v_readlane_b32 s8, v243, 7
	v_readlane_b32 s9, v243, 8
	s_load_dwordx2 s[10:11], s[8:9], 0x130
	s_load_dwordx2 s[12:13], s[8:9], 0x118
	v_mbcnt_lo_u32_b32 v150, -1, 0
	v_mbcnt_hi_u32_b32 v150, -1, v150
	v_lshrrev_b32_e32 v151, 3, v150
	v_and_b32_e32 v150, 7, v150
	v_lshlrev_b32_e32 v144, 16, v151
	v_lshl_add_u32 v144, v150, 4, v144
	v_add_u32_e32 v145, 0x1000, v144
	v_add_u32_e32 v146, 0x2000, v144
	v_add_u32_e32 v147, 0x3000, v144
	v_bfe_u32 v148, v150, 1, 1
	v_lshlrev_b32_e32 v148, 17, v148
	v_lshrrev_b32_e32 v152, 2, v150
	v_lshl_add_u32 v148, v152, 13, v148
	v_and_b32_e32 v152, 1, v150
	v_lshl_add_u32 v148, v152, 12, v148
	v_lshl_add_u32 v148, v151, 4, v148
	v_mov_b32_e32 v149, 0x43e00000
	s_mov_b32 s28, 0xc3e00000
	s_waitcnt lgkmcnt(0)
	s_add_u32 s10, s10, 0x2b00000
	s_addc_u32 s11, s11, 0
	s_lshr_b32 s22, s4, 8
	s_and_b32 s23, s4, 0xff
	s_mov_b64 s[16:17], s[12:13]
	s_add_i32 s22, s22, 0
	s_lshl_b32 s24, s22, 22
	s_lshr_b32 s25, s23, 5
	s_lshl_b32 s25, s25, 19
	s_and_b32 s26, s23, 31
	s_lshl_b32 s26, s26, 7
	s_add_i32 s24, s24, s25
	s_add_i32 s24, s24, s26
	s_add_u32 s16, s16, s24
	s_addc_u32 s17, s17, 0
	s_nop 0
	global_load_dwordx4 v[0:3], v144, s[16:17] nt
	global_load_dwordx4 v[4:7], v145, s[16:17] nt
	global_load_dwordx4 v[8:11], v146, s[16:17] nt
	global_load_dwordx4 v[12:15], v147, s[16:17] nt
	s_add_u32 s16, s16, 0x4000
	s_addc_u32 s17, s17, 0
	s_nop 0
	global_load_dwordx4 v[16:19], v144, s[16:17] nt
	global_load_dwordx4 v[20:23], v145, s[16:17] nt
	global_load_dwordx4 v[24:27], v146, s[16:17] nt
	global_load_dwordx4 v[28:31], v147, s[16:17] nt
	s_add_u32 s16, s16, 0x4000
	s_addc_u32 s17, s17, 0
	s_nop 0
	global_load_dwordx4 v[32:35], v144, s[16:17] nt
	global_load_dwordx4 v[36:39], v145, s[16:17] nt
	global_load_dwordx4 v[40:43], v146, s[16:17] nt
	global_load_dwordx4 v[44:47], v147, s[16:17] nt
	s_add_u32 s16, s16, 0x4000
	s_addc_u32 s17, s17, 0
	s_nop 0
	global_load_dwordx4 v[48:51], v144, s[16:17] nt
	global_load_dwordx4 v[52:55], v145, s[16:17] nt
	global_load_dwordx4 v[56:59], v146, s[16:17] nt
	global_load_dwordx4 v[60:63], v147, s[16:17] nt
	s_add_i32 s7, s4, s5
	s_cmp_lt_u32 s7, s6
	s_cbranch_scc0 .Lp6c0_p_last
	s_lshr_b32 s22, s7, 8
	s_and_b32 s23, s7, 0xff
	s_mov_b64 s[16:17], s[12:13]
	s_add_i32 s22, s22, 0
	s_lshl_b32 s24, s22, 22
	s_lshr_b32 s25, s23, 5
	s_lshl_b32 s25, s25, 19
	s_and_b32 s26, s23, 31
	s_lshl_b32 s26, s26, 7
	s_add_i32 s24, s24, s25
	s_add_i32 s24, s24, s26
	s_add_u32 s16, s16, s24
	s_addc_u32 s17, s17, 0
	s_nop 0
	global_load_dwordx4 v[64:67], v144, s[16:17] nt
	global_load_dwordx4 v[68:71], v145, s[16:17] nt
	global_load_dwordx4 v[72:75], v146, s[16:17] nt
	global_load_dwordx4 v[76:79], v147, s[16:17] nt
	s_add_u32 s16, s16, 0x4000
	s_addc_u32 s17, s17, 0
	s_nop 0
	global_load_dwordx4 v[80:83], v144, s[16:17] nt
	global_load_dwordx4 v[84:87], v145, s[16:17] nt
	global_load_dwordx4 v[88:91], v146, s[16:17] nt
	global_load_dwordx4 v[92:95], v147, s[16:17] nt
	s_add_u32 s16, s16, 0x4000
	s_addc_u32 s17, s17, 0
	s_nop 0
	global_load_dwordx4 v[96:99], v144, s[16:17] nt
	global_load_dwordx4 v[100:103], v145, s[16:17] nt
	global_load_dwordx4 v[104:107], v146, s[16:17] nt
	global_load_dwordx4 v[108:111], v147, s[16:17] nt
	s_add_u32 s16, s16, 0x4000
	s_addc_u32 s17, s17, 0
	s_nop 0
	global_load_dwordx4 v[112:115], v144, s[16:17] nt
	global_load_dwordx4 v[116:119], v145, s[16:17] nt
	global_load_dwordx4 v[120:123], v146, s[16:17] nt
	global_load_dwordx4 v[124:127], v147, s[16:17] nt
	s_waitcnt vmcnt(16)
	s_branch .Lp6c0_p_st

.Lp6c0_p_st:
	s_lshr_b32 s22, s4, 8
	s_and_b32 s23, s4, 0xff
	s_add_i32 s22, s22, 0
	s_mul_i32 s24, s22, 0x300000
	s_lshr_b32 s25, s23, 5
	s_lshl_b32 s25, s25, 7
	s_add_i32 s24, s24, s25
	s_and_b32 s26, s23, 31
	s_lshr_b32 s25, s26, 3
	s_lshl_b32 s25, s25, 18
	s_add_i32 s24, s24, s25
	s_bfe_u32 s25, s26, 0x20001
	s_lshl_b32 s25, s25, 15
	s_add_i32 s24, s24, s25
	s_and_b32 s25, s26, 1
	s_lshl_b32 s25, s25, 14
	s_add_i32 s24, s24, s25
	s_add_u32 s20, s10, s24
	s_addc_u32 s21, s11, 0
	v_mul_f32_e32 v0, 0x42000000, v0
	v_mul_f32_e32 v4, 0x42000000, v4
	v_mul_f32_e32 v8, 0x42000000, v8
	v_mul_f32_e32 v12, 0x42000000, v12
	v_mul_f32_e32 v16, 0x42000000, v16
	v_mul_f32_e32 v20, 0x42000000, v20
	v_mul_f32_e32 v24, 0x42000000, v24
	v_mul_f32_e32 v28, 0x42000000, v28
	v_mul_f32_e32 v32, 0x42000000, v32
	v_mul_f32_e32 v36, 0x42000000, v36
	v_mul_f32_e32 v40, 0x42000000, v40
	v_mul_f32_e32 v44, 0x42000000, v44
	v_mul_f32_e32 v48, 0x42000000, v48
	v_mul_f32_e32 v52, 0x42000000, v52
	v_mul_f32_e32 v56, 0x42000000, v56
	v_mul_f32_e32 v60, 0x42000000, v60
	v_med3_f32 v0, v0, s28, v149
	v_med3_f32 v4, v4, s28, v149
	v_med3_f32 v8, v8, s28, v149
	v_med3_f32 v12, v12, s28, v149
	v_med3_f32 v16, v16, s28, v149
	v_med3_f32 v20, v20, s28, v149
	v_med3_f32 v24, v24, s28, v149
	v_med3_f32 v28, v28, s28, v149
	v_med3_f32 v32, v32, s28, v149
	v_med3_f32 v36, v36, s28, v149
	v_med3_f32 v40, v40, s28, v149
	v_med3_f32 v44, v44, s28, v149
	v_med3_f32 v48, v48, s28, v149
	v_med3_f32 v52, v52, s28, v149
	v_med3_f32 v56, v56, s28, v149
	v_med3_f32 v60, v60, s28, v149
	v_cvt_pk_fp8_f32 v136, v0, v4
	v_cvt_pk_fp8_f32 v137, v16, v20
	v_cvt_pk_fp8_f32 v138, v32, v36
	v_cvt_pk_fp8_f32 v139, v48, v52
	v_cvt_pk_fp8_f32 v136, v8, v12 op_sel:[0,0,1]
	v_cvt_pk_fp8_f32 v137, v24, v28 op_sel:[0,0,1]
	v_cvt_pk_fp8_f32 v138, v40, v44 op_sel:[0,0,1]
	v_cvt_pk_fp8_f32 v139, v56, v60 op_sel:[0,0,1]
	s_nop 0
	global_store_dwordx4 v148, v[136:139], s[20:21]
	v_mul_f32_e32 v1, 0x42000000, v1
	v_mul_f32_e32 v5, 0x42000000, v5
	v_mul_f32_e32 v9, 0x42000000, v9
	v_mul_f32_e32 v13, 0x42000000, v13
	v_mul_f32_e32 v17, 0x42000000, v17
	v_mul_f32_e32 v21, 0x42000000, v21
	v_mul_f32_e32 v25, 0x42000000, v25
	v_mul_f32_e32 v29, 0x42000000, v29
	v_mul_f32_e32 v33, 0x42000000, v33
	v_mul_f32_e32 v37, 0x42000000, v37
	v_mul_f32_e32 v41, 0x42000000, v41
	v_mul_f32_e32 v45, 0x42000000, v45
	v_mul_f32_e32 v49, 0x42000000, v49
	v_mul_f32_e32 v53, 0x42000000, v53
	v_mul_f32_e32 v57, 0x42000000, v57
	v_mul_f32_e32 v61, 0x42000000, v61
	v_med3_f32 v1, v1, s28, v149
	v_med3_f32 v5, v5, s28, v149
	v_med3_f32 v9, v9, s28, v149
	v_med3_f32 v13, v13, s28, v149
	v_med3_f32 v17, v17, s28, v149
	v_med3_f32 v21, v21, s28, v149
	v_med3_f32 v25, v25, s28, v149
	v_med3_f32 v29, v29, s28, v149
	v_med3_f32 v33, v33, s28, v149
	v_med3_f32 v37, v37, s28, v149
	v_med3_f32 v41, v41, s28, v149
	v_med3_f32 v45, v45, s28, v149
	v_med3_f32 v49, v49, s28, v149
	v_med3_f32 v53, v53, s28, v149
	v_med3_f32 v57, v57, s28, v149
	v_med3_f32 v61, v61, s28, v149
	v_cvt_pk_fp8_f32 v140, v1, v5
	v_cvt_pk_fp8_f32 v141, v17, v21
	v_cvt_pk_fp8_f32 v142, v33, v37
	v_cvt_pk_fp8_f32 v143, v49, v53
	v_cvt_pk_fp8_f32 v140, v9, v13 op_sel:[0,0,1]
	v_cvt_pk_fp8_f32 v141, v25, v29 op_sel:[0,0,1]
	v_cvt_pk_fp8_f32 v142, v41, v45 op_sel:[0,0,1]
	v_cvt_pk_fp8_f32 v143, v57, v61 op_sel:[0,0,1]
	s_nop 0
	global_store_dwordx4 v148, v[140:143], s[20:21] offset:1024
	v_mul_f32_e32 v2, 0x42000000, v2
	v_mul_f32_e32 v6, 0x42000000, v6
	v_mul_f32_e32 v10, 0x42000000, v10
	v_mul_f32_e32 v14, 0x42000000, v14
	v_mul_f32_e32 v18, 0x42000000, v18
	v_mul_f32_e32 v22, 0x42000000, v22
	v_mul_f32_e32 v26, 0x42000000, v26
	v_mul_f32_e32 v30, 0x42000000, v30
	v_mul_f32_e32 v34, 0x42000000, v34
	v_mul_f32_e32 v38, 0x42000000, v38
	v_mul_f32_e32 v42, 0x42000000, v42
	v_mul_f32_e32 v46, 0x42000000, v46
	v_mul_f32_e32 v50, 0x42000000, v50
	v_mul_f32_e32 v54, 0x42000000, v54
	v_mul_f32_e32 v58, 0x42000000, v58
	v_mul_f32_e32 v62, 0x42000000, v62
	v_med3_f32 v2, v2, s28, v149
	v_med3_f32 v6, v6, s28, v149
	v_med3_f32 v10, v10, s28, v149
	v_med3_f32 v14, v14, s28, v149
	v_med3_f32 v18, v18, s28, v149
	v_med3_f32 v22, v22, s28, v149
	v_med3_f32 v26, v26, s28, v149
	v_med3_f32 v30, v30, s28, v149
	v_med3_f32 v34, v34, s28, v149
	v_med3_f32 v38, v38, s28, v149
	v_med3_f32 v42, v42, s28, v149
	v_med3_f32 v46, v46, s28, v149
	v_med3_f32 v50, v50, s28, v149
	v_med3_f32 v54, v54, s28, v149
	v_med3_f32 v58, v58, s28, v149
	v_med3_f32 v62, v62, s28, v149
	v_cvt_pk_fp8_f32 v136, v2, v6
	v_cvt_pk_fp8_f32 v137, v18, v22
	v_cvt_pk_fp8_f32 v138, v34, v38
	v_cvt_pk_fp8_f32 v139, v50, v54
	v_cvt_pk_fp8_f32 v136, v10, v14 op_sel:[0,0,1]
	v_cvt_pk_fp8_f32 v137, v26, v30 op_sel:[0,0,1]
	v_cvt_pk_fp8_f32 v138, v42, v46 op_sel:[0,0,1]
	v_cvt_pk_fp8_f32 v139, v58, v62 op_sel:[0,0,1]
	s_nop 0
	global_store_dwordx4 v148, v[136:139], s[20:21] offset:2048
	v_mul_f32_e32 v3, 0x42000000, v3
	v_mul_f32_e32 v7, 0x42000000, v7
	v_mul_f32_e32 v11, 0x42000000, v11
	v_mul_f32_e32 v15, 0x42000000, v15
	v_mul_f32_e32 v19, 0x42000000, v19
	v_mul_f32_e32 v23, 0x42000000, v23
	v_mul_f32_e32 v27, 0x42000000, v27
	v_mul_f32_e32 v31, 0x42000000, v31
	v_mul_f32_e32 v35, 0x42000000, v35
	v_mul_f32_e32 v39, 0x42000000, v39
	v_mul_f32_e32 v43, 0x42000000, v43
	v_mul_f32_e32 v47, 0x42000000, v47
	v_mul_f32_e32 v51, 0x42000000, v51
	v_mul_f32_e32 v55, 0x42000000, v55
	v_mul_f32_e32 v59, 0x42000000, v59
	v_mul_f32_e32 v63, 0x42000000, v63
	v_med3_f32 v3, v3, s28, v149
	v_med3_f32 v7, v7, s28, v149
	v_med3_f32 v11, v11, s28, v149
	v_med3_f32 v15, v15, s28, v149
	v_med3_f32 v19, v19, s28, v149
	v_med3_f32 v23, v23, s28, v149
	v_med3_f32 v27, v27, s28, v149
	v_med3_f32 v31, v31, s28, v149
	v_med3_f32 v35, v35, s28, v149
	v_med3_f32 v39, v39, s28, v149
	v_med3_f32 v43, v43, s28, v149
	v_med3_f32 v47, v47, s28, v149
	v_med3_f32 v51, v51, s28, v149
	v_med3_f32 v55, v55, s28, v149
	v_med3_f32 v59, v59, s28, v149
	v_med3_f32 v63, v63, s28, v149
	v_cvt_pk_fp8_f32 v140, v3, v7
	v_cvt_pk_fp8_f32 v141, v19, v23
	v_cvt_pk_fp8_f32 v142, v35, v39
	v_cvt_pk_fp8_f32 v143, v51, v55
	v_cvt_pk_fp8_f32 v140, v11, v15 op_sel:[0,0,1]
	v_cvt_pk_fp8_f32 v141, v27, v31 op_sel:[0,0,1]
	v_cvt_pk_fp8_f32 v142, v43, v47 op_sel:[0,0,1]
	v_cvt_pk_fp8_f32 v143, v59, v63 op_sel:[0,0,1]
	s_nop 0
	global_store_dwordx4 v148, v[140:143], s[20:21] offset:3072
	s_cmp_ge_u32 s7, s6
	s_cbranch_scc1 .Lp6c0_done
	s_mov_b32 s4, s7
.Lp6c0_loop:
	s_add_i32 s7, s4, s5
	s_cmp_lt_u32 s7, s6
	s_cbranch_scc0 .Lp6c0_B_last
	s_lshr_b32 s22, s7, 8
	s_and_b32 s23, s7, 0xff
	s_mov_b64 s[16:17], s[12:13]
	s_add_i32 s22, s22, 0
	s_lshl_b32 s24, s22, 22
	s_lshr_b32 s25, s23, 5
	s_lshl_b32 s25, s25, 19
	s_and_b32 s26, s23, 31
	s_lshl_b32 s26, s26, 7
	s_add_i32 s24, s24, s25
	s_add_i32 s24, s24, s26
	s_add_u32 s16, s16, s24
	s_addc_u32 s17, s17, 0
	s_nop 0
	global_load_dwordx4 v[0:3], v144, s[16:17] nt
	global_load_dwordx4 v[4:7], v145, s[16:17] nt
	global_load_dwordx4 v[8:11], v146, s[16:17] nt
	global_load_dwordx4 v[12:15], v147, s[16:17] nt
	s_add_u32 s16, s16, 0x4000
	s_addc_u32 s17, s17, 0
	s_nop 0
	global_load_dwordx4 v[16:19], v144, s[16:17] nt
	global_load_dwordx4 v[20:23], v145, s[16:17] nt
	global_load_dwordx4 v[24:27], v146, s[16:17] nt
	global_load_dwordx4 v[28:31], v147, s[16:17] nt
	s_add_u32 s16, s16, 0x4000
	s_addc_u32 s17, s17, 0
	s_nop 0
	global_load_dwordx4 v[32:35], v144, s[16:17] nt
	global_load_dwordx4 v[36:39], v145, s[16:17] nt
	global_load_dwordx4 v[40:43], v146, s[16:17] nt
	global_load_dwordx4 v[44:47], v147, s[16:17] nt
	s_add_u32 s16, s16, 0x4000
	s_addc_u32 s17, s17, 0
	s_nop 0
	global_load_dwordx4 v[48:51], v144, s[16:17] nt
	global_load_dwordx4 v[52:55], v145, s[16:17] nt
	global_load_dwordx4 v[56:59], v146, s[16:17] nt
	global_load_dwordx4 v[60:63], v147, s[16:17] nt
	s_waitcnt vmcnt(20)
	s_branch .Lp6c0_B_st

.Lp6c0_B_st:
	s_lshr_b32 s22, s4, 8
	s_and_b32 s23, s4, 0xff
	s_add_i32 s22, s22, 0
	s_mul_i32 s24, s22, 0x300000
	s_lshr_b32 s25, s23, 5
	s_lshl_b32 s25, s25, 7
	s_add_i32 s24, s24, s25
	s_and_b32 s26, s23, 31
	s_lshr_b32 s25, s26, 3
	s_lshl_b32 s25, s25, 18
	s_add_i32 s24, s24, s25
	s_bfe_u32 s25, s26, 0x20001
	s_lshl_b32 s25, s25, 15
	s_add_i32 s24, s24, s25
	s_and_b32 s25, s26, 1
	s_lshl_b32 s25, s25, 14
	s_add_i32 s24, s24, s25
	s_add_u32 s20, s10, s24
	s_addc_u32 s21, s11, 0
	v_mul_f32_e32 v64, 0x42000000, v64
	v_mul_f32_e32 v68, 0x42000000, v68
	v_mul_f32_e32 v72, 0x42000000, v72
	v_mul_f32_e32 v76, 0x42000000, v76
	v_mul_f32_e32 v80, 0x42000000, v80
	v_mul_f32_e32 v84, 0x42000000, v84
	v_mul_f32_e32 v88, 0x42000000, v88
	v_mul_f32_e32 v92, 0x42000000, v92
	v_mul_f32_e32 v96, 0x42000000, v96
	v_mul_f32_e32 v100, 0x42000000, v100
	v_mul_f32_e32 v104, 0x42000000, v104
	v_mul_f32_e32 v108, 0x42000000, v108
	v_mul_f32_e32 v112, 0x42000000, v112
	v_mul_f32_e32 v116, 0x42000000, v116
	v_mul_f32_e32 v120, 0x42000000, v120
	v_mul_f32_e32 v124, 0x42000000, v124
	v_med3_f32 v64, v64, s28, v149
	v_med3_f32 v68, v68, s28, v149
	v_med3_f32 v72, v72, s28, v149
	v_med3_f32 v76, v76, s28, v149
	v_med3_f32 v80, v80, s28, v149
	v_med3_f32 v84, v84, s28, v149
	v_med3_f32 v88, v88, s28, v149
	v_med3_f32 v92, v92, s28, v149
	v_med3_f32 v96, v96, s28, v149
	v_med3_f32 v100, v100, s28, v149
	v_med3_f32 v104, v104, s28, v149
	v_med3_f32 v108, v108, s28, v149
	v_med3_f32 v112, v112, s28, v149
	v_med3_f32 v116, v116, s28, v149
	v_med3_f32 v120, v120, s28, v149
	v_med3_f32 v124, v124, s28, v149
	v_cvt_pk_fp8_f32 v136, v64, v68
	v_cvt_pk_fp8_f32 v137, v80, v84
	v_cvt_pk_fp8_f32 v138, v96, v100
	v_cvt_pk_fp8_f32 v139, v112, v116
	v_cvt_pk_fp8_f32 v136, v72, v76 op_sel:[0,0,1]
	v_cvt_pk_fp8_f32 v137, v88, v92 op_sel:[0,0,1]
	v_cvt_pk_fp8_f32 v138, v104, v108 op_sel:[0,0,1]
	v_cvt_pk_fp8_f32 v139, v120, v124 op_sel:[0,0,1]
	s_nop 0
	global_store_dwordx4 v148, v[136:139], s[20:21]
	v_mul_f32_e32 v65, 0x42000000, v65
	v_mul_f32_e32 v69, 0x42000000, v69
	v_mul_f32_e32 v73, 0x42000000, v73
	v_mul_f32_e32 v77, 0x42000000, v77
	v_mul_f32_e32 v81, 0x42000000, v81
	v_mul_f32_e32 v85, 0x42000000, v85
	v_mul_f32_e32 v89, 0x42000000, v89
	v_mul_f32_e32 v93, 0x42000000, v93
	v_mul_f32_e32 v97, 0x42000000, v97
	v_mul_f32_e32 v101, 0x42000000, v101
	v_mul_f32_e32 v105, 0x42000000, v105
	v_mul_f32_e32 v109, 0x42000000, v109
	v_mul_f32_e32 v113, 0x42000000, v113
	v_mul_f32_e32 v117, 0x42000000, v117
	v_mul_f32_e32 v121, 0x42000000, v121
	v_mul_f32_e32 v125, 0x42000000, v125
	v_med3_f32 v65, v65, s28, v149
	v_med3_f32 v69, v69, s28, v149
	v_med3_f32 v73, v73, s28, v149
	v_med3_f32 v77, v77, s28, v149
	v_med3_f32 v81, v81, s28, v149
	v_med3_f32 v85, v85, s28, v149
	v_med3_f32 v89, v89, s28, v149
	v_med3_f32 v93, v93, s28, v149
	v_med3_f32 v97, v97, s28, v149
	v_med3_f32 v101, v101, s28, v149
	v_med3_f32 v105, v105, s28, v149
	v_med3_f32 v109, v109, s28, v149
	v_med3_f32 v113, v113, s28, v149
	v_med3_f32 v117, v117, s28, v149
	v_med3_f32 v121, v121, s28, v149
	v_med3_f32 v125, v125, s28, v149
	v_cvt_pk_fp8_f32 v140, v65, v69
	v_cvt_pk_fp8_f32 v141, v81, v85
	v_cvt_pk_fp8_f32 v142, v97, v101
	v_cvt_pk_fp8_f32 v143, v113, v117
	v_cvt_pk_fp8_f32 v140, v73, v77 op_sel:[0,0,1]
	v_cvt_pk_fp8_f32 v141, v89, v93 op_sel:[0,0,1]
	v_cvt_pk_fp8_f32 v142, v105, v109 op_sel:[0,0,1]
	v_cvt_pk_fp8_f32 v143, v121, v125 op_sel:[0,0,1]
	s_nop 0
	global_store_dwordx4 v148, v[140:143], s[20:21] offset:1024
	v_mul_f32_e32 v66, 0x42000000, v66
	v_mul_f32_e32 v70, 0x42000000, v70
	v_mul_f32_e32 v74, 0x42000000, v74
	v_mul_f32_e32 v78, 0x42000000, v78
	v_mul_f32_e32 v82, 0x42000000, v82
	v_mul_f32_e32 v86, 0x42000000, v86
	v_mul_f32_e32 v90, 0x42000000, v90
	v_mul_f32_e32 v94, 0x42000000, v94
	v_mul_f32_e32 v98, 0x42000000, v98
	v_mul_f32_e32 v102, 0x42000000, v102
	v_mul_f32_e32 v106, 0x42000000, v106
	v_mul_f32_e32 v110, 0x42000000, v110
	v_mul_f32_e32 v114, 0x42000000, v114
	v_mul_f32_e32 v118, 0x42000000, v118
	v_mul_f32_e32 v122, 0x42000000, v122
	v_mul_f32_e32 v126, 0x42000000, v126
	v_med3_f32 v66, v66, s28, v149
	v_med3_f32 v70, v70, s28, v149
	v_med3_f32 v74, v74, s28, v149
	v_med3_f32 v78, v78, s28, v149
	v_med3_f32 v82, v82, s28, v149
	v_med3_f32 v86, v86, s28, v149
	v_med3_f32 v90, v90, s28, v149
	v_med3_f32 v94, v94, s28, v149
	v_med3_f32 v98, v98, s28, v149
	v_med3_f32 v102, v102, s28, v149
	v_med3_f32 v106, v106, s28, v149
	v_med3_f32 v110, v110, s28, v149
	v_med3_f32 v114, v114, s28, v149
	v_med3_f32 v118, v118, s28, v149
	v_med3_f32 v122, v122, s28, v149
	v_med3_f32 v126, v126, s28, v149
	v_cvt_pk_fp8_f32 v136, v66, v70
	v_cvt_pk_fp8_f32 v137, v82, v86
	v_cvt_pk_fp8_f32 v138, v98, v102
	v_cvt_pk_fp8_f32 v139, v114, v118
	v_cvt_pk_fp8_f32 v136, v74, v78 op_sel:[0,0,1]
	v_cvt_pk_fp8_f32 v137, v90, v94 op_sel:[0,0,1]
	v_cvt_pk_fp8_f32 v138, v106, v110 op_sel:[0,0,1]
	v_cvt_pk_fp8_f32 v139, v122, v126 op_sel:[0,0,1]
	s_nop 0
	global_store_dwordx4 v148, v[136:139], s[20:21] offset:2048
	v_mul_f32_e32 v67, 0x42000000, v67
	v_mul_f32_e32 v71, 0x42000000, v71
	v_mul_f32_e32 v75, 0x42000000, v75
	v_mul_f32_e32 v79, 0x42000000, v79
	v_mul_f32_e32 v83, 0x42000000, v83
	v_mul_f32_e32 v87, 0x42000000, v87
	v_mul_f32_e32 v91, 0x42000000, v91
	v_mul_f32_e32 v95, 0x42000000, v95
	v_mul_f32_e32 v99, 0x42000000, v99
	v_mul_f32_e32 v103, 0x42000000, v103
	v_mul_f32_e32 v107, 0x42000000, v107
	v_mul_f32_e32 v111, 0x42000000, v111
	v_mul_f32_e32 v115, 0x42000000, v115
	v_mul_f32_e32 v119, 0x42000000, v119
	v_mul_f32_e32 v123, 0x42000000, v123
	v_mul_f32_e32 v127, 0x42000000, v127
	v_med3_f32 v67, v67, s28, v149
	v_med3_f32 v71, v71, s28, v149
	v_med3_f32 v75, v75, s28, v149
	v_med3_f32 v79, v79, s28, v149
	v_med3_f32 v83, v83, s28, v149
	v_med3_f32 v87, v87, s28, v149
	v_med3_f32 v91, v91, s28, v149
	v_med3_f32 v95, v95, s28, v149
	v_med3_f32 v99, v99, s28, v149
	v_med3_f32 v103, v103, s28, v149
	v_med3_f32 v107, v107, s28, v149
	v_med3_f32 v111, v111, s28, v149
	v_med3_f32 v115, v115, s28, v149
	v_med3_f32 v119, v119, s28, v149
	v_med3_f32 v123, v123, s28, v149
	v_med3_f32 v127, v127, s28, v149
	v_cvt_pk_fp8_f32 v140, v67, v71
	v_cvt_pk_fp8_f32 v141, v83, v87
	v_cvt_pk_fp8_f32 v142, v99, v103
	v_cvt_pk_fp8_f32 v143, v115, v119
	v_cvt_pk_fp8_f32 v140, v75, v79 op_sel:[0,0,1]
	v_cvt_pk_fp8_f32 v141, v91, v95 op_sel:[0,0,1]
	v_cvt_pk_fp8_f32 v142, v107, v111 op_sel:[0,0,1]
	v_cvt_pk_fp8_f32 v143, v123, v127 op_sel:[0,0,1]
	s_nop 0
	global_store_dwordx4 v148, v[140:143], s[20:21] offset:3072
	s_cmp_ge_u32 s7, s6
	s_cbranch_scc1 .Lp6c0_done
	s_mov_b32 s4, s7
	s_add_i32 s7, s4, s5
	s_cmp_lt_u32 s7, s6
	s_cbranch_scc0 .Lp6c0_A_last
	s_lshr_b32 s22, s7, 8
	s_and_b32 s23, s7, 0xff
	s_mov_b64 s[16:17], s[12:13]
	s_add_i32 s22, s22, 0
	s_lshl_b32 s24, s22, 22
	s_lshr_b32 s25, s23, 5
	s_lshl_b32 s25, s25, 19
	s_and_b32 s26, s23, 31
	s_lshl_b32 s26, s26, 7
	s_add_i32 s24, s24, s25
	s_add_i32 s24, s24, s26
	s_add_u32 s16, s16, s24
	s_addc_u32 s17, s17, 0
	s_nop 0
	global_load_dwordx4 v[64:67], v144, s[16:17] nt
	global_load_dwordx4 v[68:71], v145, s[16:17] nt
	global_load_dwordx4 v[72:75], v146, s[16:17] nt
	global_load_dwordx4 v[76:79], v147, s[16:17] nt
	s_add_u32 s16, s16, 0x4000
	s_addc_u32 s17, s17, 0
	s_nop 0
	global_load_dwordx4 v[80:83], v144, s[16:17] nt
	global_load_dwordx4 v[84:87], v145, s[16:17] nt
	global_load_dwordx4 v[88:91], v146, s[16:17] nt
	global_load_dwordx4 v[92:95], v147, s[16:17] nt
	s_add_u32 s16, s16, 0x4000
	s_addc_u32 s17, s17, 0
	s_nop 0
	global_load_dwordx4 v[96:99], v144, s[16:17] nt
	global_load_dwordx4 v[100:103], v145, s[16:17] nt
	global_load_dwordx4 v[104:107], v146, s[16:17] nt
	global_load_dwordx4 v[108:111], v147, s[16:17] nt
	s_add_u32 s16, s16, 0x4000
	s_addc_u32 s17, s17, 0
	s_nop 0
	global_load_dwordx4 v[112:115], v144, s[16:17] nt
	global_load_dwordx4 v[116:119], v145, s[16:17] nt
	global_load_dwordx4 v[120:123], v146, s[16:17] nt
	global_load_dwordx4 v[124:127], v147, s[16:17] nt
	s_waitcnt vmcnt(20)
	s_branch .Lp6c0_A_st

.Lp6c0_A_st:
	s_lshr_b32 s22, s4, 8
	s_and_b32 s23, s4, 0xff
	s_add_i32 s22, s22, 0
	s_mul_i32 s24, s22, 0x300000
	s_lshr_b32 s25, s23, 5
	s_lshl_b32 s25, s25, 7
	s_add_i32 s24, s24, s25
	s_and_b32 s26, s23, 31
	s_lshr_b32 s25, s26, 3
	s_lshl_b32 s25, s25, 18
	s_add_i32 s24, s24, s25
	s_bfe_u32 s25, s26, 0x20001
	s_lshl_b32 s25, s25, 15
	s_add_i32 s24, s24, s25
	s_and_b32 s25, s26, 1
	s_lshl_b32 s25, s25, 14
	s_add_i32 s24, s24, s25
	s_add_u32 s20, s10, s24
	s_addc_u32 s21, s11, 0
	v_mul_f32_e32 v0, 0x42000000, v0
	v_mul_f32_e32 v4, 0x42000000, v4
	v_mul_f32_e32 v8, 0x42000000, v8
	v_mul_f32_e32 v12, 0x42000000, v12
	v_mul_f32_e32 v16, 0x42000000, v16
	v_mul_f32_e32 v20, 0x42000000, v20
	v_mul_f32_e32 v24, 0x42000000, v24
	v_mul_f32_e32 v28, 0x42000000, v28
	v_mul_f32_e32 v32, 0x42000000, v32
	v_mul_f32_e32 v36, 0x42000000, v36
	v_mul_f32_e32 v40, 0x42000000, v40
	v_mul_f32_e32 v44, 0x42000000, v44
	v_mul_f32_e32 v48, 0x42000000, v48
	v_mul_f32_e32 v52, 0x42000000, v52
	v_mul_f32_e32 v56, 0x42000000, v56
	v_mul_f32_e32 v60, 0x42000000, v60
	v_med3_f32 v0, v0, s28, v149
	v_med3_f32 v4, v4, s28, v149
	v_med3_f32 v8, v8, s28, v149
	v_med3_f32 v12, v12, s28, v149
	v_med3_f32 v16, v16, s28, v149
	v_med3_f32 v20, v20, s28, v149
	v_med3_f32 v24, v24, s28, v149
	v_med3_f32 v28, v28, s28, v149
	v_med3_f32 v32, v32, s28, v149
	v_med3_f32 v36, v36, s28, v149
	v_med3_f32 v40, v40, s28, v149
	v_med3_f32 v44, v44, s28, v149
	v_med3_f32 v48, v48, s28, v149
	v_med3_f32 v52, v52, s28, v149
	v_med3_f32 v56, v56, s28, v149
	v_med3_f32 v60, v60, s28, v149
	v_cvt_pk_fp8_f32 v136, v0, v4
	v_cvt_pk_fp8_f32 v137, v16, v20
	v_cvt_pk_fp8_f32 v138, v32, v36
	v_cvt_pk_fp8_f32 v139, v48, v52
	v_cvt_pk_fp8_f32 v136, v8, v12 op_sel:[0,0,1]
	v_cvt_pk_fp8_f32 v137, v24, v28 op_sel:[0,0,1]
	v_cvt_pk_fp8_f32 v138, v40, v44 op_sel:[0,0,1]
	v_cvt_pk_fp8_f32 v139, v56, v60 op_sel:[0,0,1]
	s_nop 0
	global_store_dwordx4 v148, v[136:139], s[20:21]
	v_mul_f32_e32 v1, 0x42000000, v1
	v_mul_f32_e32 v5, 0x42000000, v5
	v_mul_f32_e32 v9, 0x42000000, v9
	v_mul_f32_e32 v13, 0x42000000, v13
	v_mul_f32_e32 v17, 0x42000000, v17
	v_mul_f32_e32 v21, 0x42000000, v21
	v_mul_f32_e32 v25, 0x42000000, v25
	v_mul_f32_e32 v29, 0x42000000, v29
	v_mul_f32_e32 v33, 0x42000000, v33
	v_mul_f32_e32 v37, 0x42000000, v37
	v_mul_f32_e32 v41, 0x42000000, v41
	v_mul_f32_e32 v45, 0x42000000, v45
	v_mul_f32_e32 v49, 0x42000000, v49
	v_mul_f32_e32 v53, 0x42000000, v53
	v_mul_f32_e32 v57, 0x42000000, v57
	v_mul_f32_e32 v61, 0x42000000, v61
	v_med3_f32 v1, v1, s28, v149
	v_med3_f32 v5, v5, s28, v149
	v_med3_f32 v9, v9, s28, v149
	v_med3_f32 v13, v13, s28, v149
	v_med3_f32 v17, v17, s28, v149
	v_med3_f32 v21, v21, s28, v149
	v_med3_f32 v25, v25, s28, v149
	v_med3_f32 v29, v29, s28, v149
	v_med3_f32 v33, v33, s28, v149
	v_med3_f32 v37, v37, s28, v149
	v_med3_f32 v41, v41, s28, v149
	v_med3_f32 v45, v45, s28, v149
	v_med3_f32 v49, v49, s28, v149
	v_med3_f32 v53, v53, s28, v149
	v_med3_f32 v57, v57, s28, v149
	v_med3_f32 v61, v61, s28, v149
	v_cvt_pk_fp8_f32 v140, v1, v5
	v_cvt_pk_fp8_f32 v141, v17, v21
	v_cvt_pk_fp8_f32 v142, v33, v37
	v_cvt_pk_fp8_f32 v143, v49, v53
	v_cvt_pk_fp8_f32 v140, v9, v13 op_sel:[0,0,1]
	v_cvt_pk_fp8_f32 v141, v25, v29 op_sel:[0,0,1]
	v_cvt_pk_fp8_f32 v142, v41, v45 op_sel:[0,0,1]
	v_cvt_pk_fp8_f32 v143, v57, v61 op_sel:[0,0,1]
	s_nop 0
	global_store_dwordx4 v148, v[140:143], s[20:21] offset:1024
	v_mul_f32_e32 v2, 0x42000000, v2
	v_mul_f32_e32 v6, 0x42000000, v6
	v_mul_f32_e32 v10, 0x42000000, v10
	v_mul_f32_e32 v14, 0x42000000, v14
	v_mul_f32_e32 v18, 0x42000000, v18
	v_mul_f32_e32 v22, 0x42000000, v22
	v_mul_f32_e32 v26, 0x42000000, v26
	v_mul_f32_e32 v30, 0x42000000, v30
	v_mul_f32_e32 v34, 0x42000000, v34
	v_mul_f32_e32 v38, 0x42000000, v38
	v_mul_f32_e32 v42, 0x42000000, v42
	v_mul_f32_e32 v46, 0x42000000, v46
	v_mul_f32_e32 v50, 0x42000000, v50
	v_mul_f32_e32 v54, 0x42000000, v54
	v_mul_f32_e32 v58, 0x42000000, v58
	v_mul_f32_e32 v62, 0x42000000, v62
	v_med3_f32 v2, v2, s28, v149
	v_med3_f32 v6, v6, s28, v149
	v_med3_f32 v10, v10, s28, v149
	v_med3_f32 v14, v14, s28, v149
	v_med3_f32 v18, v18, s28, v149
	v_med3_f32 v22, v22, s28, v149
	v_med3_f32 v26, v26, s28, v149
	v_med3_f32 v30, v30, s28, v149
	v_med3_f32 v34, v34, s28, v149
	v_med3_f32 v38, v38, s28, v149
	v_med3_f32 v42, v42, s28, v149
	v_med3_f32 v46, v46, s28, v149
	v_med3_f32 v50, v50, s28, v149
	v_med3_f32 v54, v54, s28, v149
	v_med3_f32 v58, v58, s28, v149
	v_med3_f32 v62, v62, s28, v149
	v_cvt_pk_fp8_f32 v136, v2, v6
	v_cvt_pk_fp8_f32 v137, v18, v22
	v_cvt_pk_fp8_f32 v138, v34, v38
	v_cvt_pk_fp8_f32 v139, v50, v54
	v_cvt_pk_fp8_f32 v136, v10, v14 op_sel:[0,0,1]
	v_cvt_pk_fp8_f32 v137, v26, v30 op_sel:[0,0,1]
	v_cvt_pk_fp8_f32 v138, v42, v46 op_sel:[0,0,1]
	v_cvt_pk_fp8_f32 v139, v58, v62 op_sel:[0,0,1]
	s_nop 0
	global_store_dwordx4 v148, v[136:139], s[20:21] offset:2048
	v_mul_f32_e32 v3, 0x42000000, v3
	v_mul_f32_e32 v7, 0x42000000, v7
	v_mul_f32_e32 v11, 0x42000000, v11
	v_mul_f32_e32 v15, 0x42000000, v15
	v_mul_f32_e32 v19, 0x42000000, v19
	v_mul_f32_e32 v23, 0x42000000, v23
	v_mul_f32_e32 v27, 0x42000000, v27
	v_mul_f32_e32 v31, 0x42000000, v31
	v_mul_f32_e32 v35, 0x42000000, v35
	v_mul_f32_e32 v39, 0x42000000, v39
	v_mul_f32_e32 v43, 0x42000000, v43
	v_mul_f32_e32 v47, 0x42000000, v47
	v_mul_f32_e32 v51, 0x42000000, v51
	v_mul_f32_e32 v55, 0x42000000, v55
	v_mul_f32_e32 v59, 0x42000000, v59
	v_mul_f32_e32 v63, 0x42000000, v63
	v_med3_f32 v3, v3, s28, v149
	v_med3_f32 v7, v7, s28, v149
	v_med3_f32 v11, v11, s28, v149
	v_med3_f32 v15, v15, s28, v149
	v_med3_f32 v19, v19, s28, v149
	v_med3_f32 v23, v23, s28, v149
	v_med3_f32 v27, v27, s28, v149
	v_med3_f32 v31, v31, s28, v149
	v_med3_f32 v35, v35, s28, v149
	v_med3_f32 v39, v39, s28, v149
	v_med3_f32 v43, v43, s28, v149
	v_med3_f32 v47, v47, s28, v149
	v_med3_f32 v51, v51, s28, v149
	v_med3_f32 v55, v55, s28, v149
	v_med3_f32 v59, v59, s28, v149
	v_med3_f32 v63, v63, s28, v149
	v_cvt_pk_fp8_f32 v140, v3, v7
	v_cvt_pk_fp8_f32 v141, v19, v23
	v_cvt_pk_fp8_f32 v142, v35, v39
	v_cvt_pk_fp8_f32 v143, v51, v55
	v_cvt_pk_fp8_f32 v140, v11, v15 op_sel:[0,0,1]
	v_cvt_pk_fp8_f32 v141, v27, v31 op_sel:[0,0,1]
	v_cvt_pk_fp8_f32 v142, v43, v47 op_sel:[0,0,1]
	v_cvt_pk_fp8_f32 v143, v59, v63 op_sel:[0,0,1]
	s_nop 0
	global_store_dwordx4 v148, v[140:143], s[20:21] offset:3072
	s_cmp_ge_u32 s7, s6
	s_cbranch_scc1 .Lp6c0_done
	s_mov_b32 s4, s7
	s_branch .Lp6c0_loop
.Lp6c0_done:
.LBB0_776:
	s_mov_b64 s[4:5], 0
.LBB0_777:
	v_add_u32_e32 v162, s33, v135
	s_and_b64 vcc, exec, s[4:5]
	s_cbranch_vccz .LBB0_907
	s_load_dwordx2 s[14:15], s[0:1], 0x130
	v_cmp_gt_i32_e32 vcc, 32, v162
	s_waitcnt vmcnt(0) lgkmcnt(0)
	s_barrier
	s_and_saveexec_b64 s[4:5], vcc
	s_cbranch_execz .LBB0_780
	v_lshlrev_b32_e32 v0, 6, v162
	v_ashrrev_i32_e32 v1, 31, v0
	v_lshl_add_u64 v[0:1], v[0:1], 2, s[14:15]
	v_add_co_u32_e32 v0, vcc, 0x40000, v0
	s_nop 1
	v_addc_co_u32_e32 v1, vcc, 0, v1, vcc
	global_load_dword v0, v[0:1], off sc1
	v_lshl_add_u32 v1, v162, 2, 0
	v_add_u32_e32 v1, 0x20000, v1
	s_waitcnt vmcnt(0)
	ds_write_b32 v1, v0

.LBB0_1234:
	s_load_dwordx4 s[0:3], s[8:9], 0x138
	s_waitcnt lgkmcnt(0)
	s_mov_b64 s[4:5], s[0:1]
	s_cmp_lt_i32 s4, 10
	s_cselect_b64 s[0:1], -1, 0
	s_cmp_gt_i32 s5, 9
	s_cselect_b64 s[2:3], -1, 0
	s_and_b64 s[0:1], s[0:1], s[2:3]
	s_andn2_b64 vcc, exec, s[0:1]
	s_cbranch_vccnz .LBB0_1372
	s_mov_b64 s[0:1], s[8:9]
	v_mbcnt_lo_u32_b32 v146, -1, 0
	v_mbcnt_hi_u32_b32 v146, -1, v146
	s_load_dword s38, s[8:9], 0x148
	s_add_u32 s4, s8, 0x148
	v_readlane_b32 s2, v243, 0
	s_addc_u32 s5, s9, 0
	v_readlane_b32 s3, v243, 1
	s_waitcnt lgkmcnt(0)
	s_sub_i32 s39, s38, 32
	s_cmp_lt_i32 s2, s39
	s_mov_b64 s[2:3], -1
	s_cbranch_scc1 .LBB0_1257
	s_mov_b64 s[30:31], s[4:5]
	v_readlane_b32 s4, v243, 0
	s_sub_i32 s4, s4, s39
	s_lshl_b32 s4, s4, 3
	s_add_i32 s19, s4, s94
	s_mov_b32 s4, s19
	s_mov_b32 s5, 0x100
	s_mov_b32 s6, 0x1c00
	s_waitcnt vmcnt(0)
	s_cmp_ge_u32 s4, s6
	s_cbranch_scc1 .Lp9c0_done
	v_readlane_b32 s8, v243, 7
	v_readlane_b32 s9, v243, 8
	s_load_dwordx2 s[10:11], s[8:9], 0x130
	s_load_dwordx2 s[12:13], s[8:9], 0xf8
	s_load_dwordx2 s[14:15], s[8:9], 0x108
	v_mbcnt_lo_u32_b32 v162, -1, 0
	v_mbcnt_hi_u32_b32 v162, -1, v162
	v_lshrrev_b32_e32 v163, 3, v162
	v_and_b32_e32 v162, 7, v162
	v_lshlrev_b32_e32 v156, 16, v163
	v_lshl_add_u32 v156, v162, 4, v156
	v_add_u32_e32 v157, 0x1000, v156
	v_add_u32_e32 v158, 0x2000, v156
	v_add_u32_e32 v159, 0x3000, v156
	v_lshlrev_b32_e32 v160, 12, v162
	v_lshl_add_u32 v160, v163, 4, v160
	v_mov_b32_e32 v161, 0x43e00000
	s_mov_b32 s28, 0xc3e00000
	s_waitcnt lgkmcnt(0)
	s_add_u32 s10, s10, 0x2900000
	s_addc_u32 s11, s11, 0
	s_lshr_b32 s22, s4, 8
	s_and_b32 s23, s4, 0xff
	s_and_b32 s27, s22, 1
	s_lshr_b32 s22, s22, 1
	s_cmp_eq_u32 s27, 0
	s_cselect_b64 s[16:17], s[12:13], s[14:15]
	s_add_i32 s22, s22, 50
	s_lshl_b32 s24, s22, 22
	s_lshr_b32 s25, s23, 5
	s_lshl_b32 s25, s25, 19
	s_and_b32 s26, s23, 31
	s_lshl_b32 s26, s26, 7
	s_add_i32 s24, s24, s25
	s_add_i32 s24, s24, s26
	s_add_u32 s16, s16, s24
	s_addc_u32 s17, s17, 0
	s_nop 0
	global_load_dwordx4 v[0:3], v156, s[16:17] nt
	global_load_dwordx4 v[4:7], v157, s[16:17] nt
	global_load_dwordx4 v[8:11], v158, s[16:17] nt
	global_load_dwordx4 v[12:15], v159, s[16:17] nt
	s_add_u32 s16, s16, 0x4000
	s_addc_u32 s17, s17, 0
	s_nop 0
	global_load_dwordx4 v[16:19], v156, s[16:17] nt
	global_load_dwordx4 v[20:23], v157, s[16:17] nt
	global_load_dwordx4 v[24:27], v158, s[16:17] nt
	global_load_dwordx4 v[28:31], v159, s[16:17] nt
	s_add_u32 s16, s16, 0x4000
	s_addc_u32 s17, s17, 0
	s_nop 0
	global_load_dwordx4 v[32:35], v156, s[16:17] nt
	global_load_dwordx4 v[36:39], v157, s[16:17] nt
	global_load_dwordx4 v[40:43], v158, s[16:17] nt
	global_load_dwordx4 v[44:47], v159, s[16:17] nt
	s_add_u32 s16, s16, 0x4000
	s_addc_u32 s17, s17, 0
	s_nop 0
	global_load_dwordx4 v[48:51], v156, s[16:17] nt
	global_load_dwordx4 v[52:55], v157, s[16:17] nt
	global_load_dwordx4 v[56:59], v158, s[16:17] nt
	global_load_dwordx4 v[60:63], v159, s[16:17] nt
	s_add_i32 s7, s4, s5
	s_cmp_lt_u32 s7, s6
	s_cbranch_scc0 .Lp9c0_p_last
	s_lshr_b32 s22, s7, 8
	s_and_b32 s23, s7, 0xff
	s_and_b32 s27, s22, 1
	s_lshr_b32 s22, s22, 1
	s_cmp_eq_u32 s27, 0
	s_cselect_b64 s[16:17], s[12:13], s[14:15]
	s_add_i32 s22, s22, 50
	s_lshl_b32 s24, s22, 22
	s_lshr_b32 s25, s23, 5
	s_lshl_b32 s25, s25, 19
	s_and_b32 s26, s23, 31
	s_lshl_b32 s26, s26, 7
	s_add_i32 s24, s24, s25
	s_add_i32 s24, s24, s26
	s_add_u32 s16, s16, s24
	s_addc_u32 s17, s17, 0
	s_nop 0
	global_load_dwordx4 v[64:67], v156, s[16:17] nt
	global_load_dwordx4 v[68:71], v157, s[16:17] nt
	global_load_dwordx4 v[72:75], v158, s[16:17] nt
	global_load_dwordx4 v[76:79], v159, s[16:17] nt
	s_add_u32 s16, s16, 0x4000
	s_addc_u32 s17, s17, 0
	s_nop 0
	global_load_dwordx4 v[80:83], v156, s[16:17] nt
	global_load_dwordx4 v[84:87], v157, s[16:17] nt
	global_load_dwordx4 v[88:91], v158, s[16:17] nt
	global_load_dwordx4 v[92:95], v159, s[16:17] nt
	s_add_u32 s16, s16, 0x4000
	s_addc_u32 s17, s17, 0
	s_nop 0
	global_load_dwordx4 v[96:99], v156, s[16:17] nt
	global_load_dwordx4 v[100:103], v157, s[16:17] nt
	global_load_dwordx4 v[104:107], v158, s[16:17] nt
	global_load_dwordx4 v[108:111], v159, s[16:17] nt
	s_add_u32 s16, s16, 0x4000
	s_addc_u32 s17, s17, 0
	s_nop 0
	global_load_dwordx4 v[112:115], v156, s[16:17] nt
	global_load_dwordx4 v[116:119], v157, s[16:17] nt
	global_load_dwordx4 v[120:123], v158, s[16:17] nt
	global_load_dwordx4 v[124:127], v159, s[16:17] nt
	s_waitcnt vmcnt(16)
	s_branch .Lp9c0_p_st

.Lp9c0_p_st:
	s_lshr_b32 s22, s4, 8
	s_and_b32 s23, s4, 0xff
	s_and_b32 s27, s22, 1
	s_lshr_b32 s22, s22, 1
	s_add_i32 s22, s22, 50
	s_mul_i32 s24, s22, 0x300000
	s_lshr_b32 s25, s23, 5
	s_lshl_b32 s25, s25, 7
	s_add_i32 s24, s24, s25
	s_and_b32 s26, s23, 31
	s_lshr_b32 s25, s26, 2
	s_lshl_b32 s25, s25, 18
	s_add_i32 s24, s24, s25
	s_lshl_b32 s25, s27, 17
	s_add_i32 s24, s24, s25
	s_and_b32 s25, s26, 3
	s_lshl_b32 s25, s25, 15
	s_add_i32 s24, s24, s25
	s_add_u32 s20, s10, s24
	s_addc_u32 s21, s11, 0
	v_mul_f32_e32 v0, 0x42000000, v0
	v_mul_f32_e32 v4, 0x42000000, v4
	v_mul_f32_e32 v8, 0x42000000, v8
	v_mul_f32_e32 v12, 0x42000000, v12
	v_mul_f32_e32 v16, 0x42000000, v16
	v_mul_f32_e32 v20, 0x42000000, v20
	v_mul_f32_e32 v24, 0x42000000, v24
	v_mul_f32_e32 v28, 0x42000000, v28
	v_mul_f32_e32 v32, 0x42000000, v32
	v_mul_f32_e32 v36, 0x42000000, v36
	v_mul_f32_e32 v40, 0x42000000, v40
	v_mul_f32_e32 v44, 0x42000000, v44
	v_mul_f32_e32 v48, 0x42000000, v48
	v_mul_f32_e32 v52, 0x42000000, v52
	v_mul_f32_e32 v56, 0x42000000, v56
	v_mul_f32_e32 v60, 0x42000000, v60
	v_med3_f32 v0, v0, s28, v161
	v_med3_f32 v4, v4, s28, v161
	v_med3_f32 v8, v8, s28, v161
	v_med3_f32 v12, v12, s28, v161
	v_med3_f32 v16, v16, s28, v161
	v_med3_f32 v20, v20, s28, v161
	v_med3_f32 v24, v24, s28, v161
	v_med3_f32 v28, v28, s28, v161
	v_med3_f32 v32, v32, s28, v161
	v_med3_f32 v36, v36, s28, v161
	v_med3_f32 v40, v40, s28, v161
	v_med3_f32 v44, v44, s28, v161
	v_med3_f32 v48, v48, s28, v161
	v_med3_f32 v52, v52, s28, v161
	v_med3_f32 v56, v56, s28, v161
	v_med3_f32 v60, v60, s28, v161
	v_cvt_pk_fp8_f32 v148, v0, v4
	v_cvt_pk_fp8_f32 v149, v16, v20
	v_cvt_pk_fp8_f32 v150, v32, v36
	v_cvt_pk_fp8_f32 v151, v48, v52
	v_cvt_pk_fp8_f32 v148, v8, v12 op_sel:[0,0,1]
	v_cvt_pk_fp8_f32 v149, v24, v28 op_sel:[0,0,1]
	v_cvt_pk_fp8_f32 v150, v40, v44 op_sel:[0,0,1]
	v_cvt_pk_fp8_f32 v151, v56, v60 op_sel:[0,0,1]
	s_nop 0
	global_store_dwordx4 v160, v[148:151], s[20:21]
	v_mul_f32_e32 v1, 0x42000000, v1
	v_mul_f32_e32 v5, 0x42000000, v5
	v_mul_f32_e32 v9, 0x42000000, v9
	v_mul_f32_e32 v13, 0x42000000, v13
	v_mul_f32_e32 v17, 0x42000000, v17
	v_mul_f32_e32 v21, 0x42000000, v21
	v_mul_f32_e32 v25, 0x42000000, v25
	v_mul_f32_e32 v29, 0x42000000, v29
	v_mul_f32_e32 v33, 0x42000000, v33
	v_mul_f32_e32 v37, 0x42000000, v37
	v_mul_f32_e32 v41, 0x42000000, v41
	v_mul_f32_e32 v45, 0x42000000, v45
	v_mul_f32_e32 v49, 0x42000000, v49
	v_mul_f32_e32 v53, 0x42000000, v53
	v_mul_f32_e32 v57, 0x42000000, v57
	v_mul_f32_e32 v61, 0x42000000, v61
	v_med3_f32 v1, v1, s28, v161
	v_med3_f32 v5, v5, s28, v161
	v_med3_f32 v9, v9, s28, v161
	v_med3_f32 v13, v13, s28, v161
	v_med3_f32 v17, v17, s28, v161
	v_med3_f32 v21, v21, s28, v161
	v_med3_f32 v25, v25, s28, v161
	v_med3_f32 v29, v29, s28, v161
	v_med3_f32 v33, v33, s28, v161
	v_med3_f32 v37, v37, s28, v161
	v_med3_f32 v41, v41, s28, v161
	v_med3_f32 v45, v45, s28, v161
	v_med3_f32 v49, v49, s28, v161
	v_med3_f32 v53, v53, s28, v161
	v_med3_f32 v57, v57, s28, v161
	v_med3_f32 v61, v61, s28, v161
	v_cvt_pk_fp8_f32 v152, v1, v5
	v_cvt_pk_fp8_f32 v153, v17, v21
	v_cvt_pk_fp8_f32 v154, v33, v37
	v_cvt_pk_fp8_f32 v155, v49, v53
	v_cvt_pk_fp8_f32 v152, v9, v13 op_sel:[0,0,1]
	v_cvt_pk_fp8_f32 v153, v25, v29 op_sel:[0,0,1]
	v_cvt_pk_fp8_f32 v154, v41, v45 op_sel:[0,0,1]
	v_cvt_pk_fp8_f32 v155, v57, v61 op_sel:[0,0,1]
	s_nop 0
	global_store_dwordx4 v160, v[152:155], s[20:21] offset:1024
	v_mul_f32_e32 v2, 0x42000000, v2
	v_mul_f32_e32 v6, 0x42000000, v6
	v_mul_f32_e32 v10, 0x42000000, v10
	v_mul_f32_e32 v14, 0x42000000, v14
	v_mul_f32_e32 v18, 0x42000000, v18
	v_mul_f32_e32 v22, 0x42000000, v22
	v_mul_f32_e32 v26, 0x42000000, v26
	v_mul_f32_e32 v30, 0x42000000, v30
	v_mul_f32_e32 v34, 0x42000000, v34
	v_mul_f32_e32 v38, 0x42000000, v38
	v_mul_f32_e32 v42, 0x42000000, v42
	v_mul_f32_e32 v46, 0x42000000, v46
	v_mul_f32_e32 v50, 0x42000000, v50
	v_mul_f32_e32 v54, 0x42000000, v54
	v_mul_f32_e32 v58, 0x42000000, v58
	v_mul_f32_e32 v62, 0x42000000, v62
	v_med3_f32 v2, v2, s28, v161
	v_med3_f32 v6, v6, s28, v161
	v_med3_f32 v10, v10, s28, v161
	v_med3_f32 v14, v14, s28, v161
	v_med3_f32 v18, v18, s28, v161
	v_med3_f32 v22, v22, s28, v161
	v_med3_f32 v26, v26, s28, v161
	v_med3_f32 v30, v30, s28, v161
	v_med3_f32 v34, v34, s28, v161
	v_med3_f32 v38, v38, s28, v161
	v_med3_f32 v42, v42, s28, v161
	v_med3_f32 v46, v46, s28, v161
	v_med3_f32 v50, v50, s28, v161
	v_med3_f32 v54, v54, s28, v161
	v_med3_f32 v58, v58, s28, v161
	v_med3_f32 v62, v62, s28, v161
	v_cvt_pk_fp8_f32 v148, v2, v6
	v_cvt_pk_fp8_f32 v149, v18, v22
	v_cvt_pk_fp8_f32 v150, v34, v38
	v_cvt_pk_fp8_f32 v151, v50, v54
	v_cvt_pk_fp8_f32 v148, v10, v14 op_sel:[0,0,1]
	v_cvt_pk_fp8_f32 v149, v26, v30 op_sel:[0,0,1]
	v_cvt_pk_fp8_f32 v150, v42, v46 op_sel:[0,0,1]
	v_cvt_pk_fp8_f32 v151, v58, v62 op_sel:[0,0,1]
	s_nop 0
	global_store_dwordx4 v160, v[148:151], s[20:21] offset:2048
	v_mul_f32_e32 v3, 0x42000000, v3
	v_mul_f32_e32 v7, 0x42000000, v7
	v_mul_f32_e32 v11, 0x42000000, v11
	v_mul_f32_e32 v15, 0x42000000, v15
	v_mul_f32_e32 v19, 0x42000000, v19
	v_mul_f32_e32 v23, 0x42000000, v23
	v_mul_f32_e32 v27, 0x42000000, v27
	v_mul_f32_e32 v31, 0x42000000, v31
	v_mul_f32_e32 v35, 0x42000000, v35
	v_mul_f32_e32 v39, 0x42000000, v39
	v_mul_f32_e32 v43, 0x42000000, v43
	v_mul_f32_e32 v47, 0x42000000, v47
	v_mul_f32_e32 v51, 0x42000000, v51
	v_mul_f32_e32 v55, 0x42000000, v55
	v_mul_f32_e32 v59, 0x42000000, v59
	v_mul_f32_e32 v63, 0x42000000, v63
	v_med3_f32 v3, v3, s28, v161
	v_med3_f32 v7, v7, s28, v161
	v_med3_f32 v11, v11, s28, v161
	v_med3_f32 v15, v15, s28, v161
	v_med3_f32 v19, v19, s28, v161
	v_med3_f32 v23, v23, s28, v161
	v_med3_f32 v27, v27, s28, v161
	v_med3_f32 v31, v31, s28, v161
	v_med3_f32 v35, v35, s28, v161
	v_med3_f32 v39, v39, s28, v161
	v_med3_f32 v43, v43, s28, v161
	v_med3_f32 v47, v47, s28, v161
	v_med3_f32 v51, v51, s28, v161
	v_med3_f32 v55, v55, s28, v161
	v_med3_f32 v59, v59, s28, v161
	v_med3_f32 v63, v63, s28, v161
	v_cvt_pk_fp8_f32 v152, v3, v7
	v_cvt_pk_fp8_f32 v153, v19, v23
	v_cvt_pk_fp8_f32 v154, v35, v39
	v_cvt_pk_fp8_f32 v155, v51, v55
	v_cvt_pk_fp8_f32 v152, v11, v15 op_sel:[0,0,1]
	v_cvt_pk_fp8_f32 v153, v27, v31 op_sel:[0,0,1]
	v_cvt_pk_fp8_f32 v154, v43, v47 op_sel:[0,0,1]
	v_cvt_pk_fp8_f32 v155, v59, v63 op_sel:[0,0,1]
	s_nop 0
	global_store_dwordx4 v160, v[152:155], s[20:21] offset:3072
	s_cmp_ge_u32 s7, s6
	s_cbranch_scc1 .Lp9c0_done
	s_mov_b32 s4, s7
.Lp9c0_loop:
	s_add_i32 s7, s4, s5
	s_cmp_lt_u32 s7, s6
	s_cbranch_scc0 .Lp9c0_B_last
	s_lshr_b32 s22, s7, 8
	s_and_b32 s23, s7, 0xff
	s_and_b32 s27, s22, 1
	s_lshr_b32 s22, s22, 1
	s_cmp_eq_u32 s27, 0
	s_cselect_b64 s[16:17], s[12:13], s[14:15]
	s_add_i32 s22, s22, 50
	s_lshl_b32 s24, s22, 22
	s_lshr_b32 s25, s23, 5
	s_lshl_b32 s25, s25, 19
	s_and_b32 s26, s23, 31
	s_lshl_b32 s26, s26, 7
	s_add_i32 s24, s24, s25
	s_add_i32 s24, s24, s26
	s_add_u32 s16, s16, s24
	s_addc_u32 s17, s17, 0
	s_nop 0
	global_load_dwordx4 v[0:3], v156, s[16:17] nt
	global_load_dwordx4 v[4:7], v157, s[16:17] nt
	global_load_dwordx4 v[8:11], v158, s[16:17] nt
	global_load_dwordx4 v[12:15], v159, s[16:17] nt
	s_add_u32 s16, s16, 0x4000
	s_addc_u32 s17, s17, 0
	s_nop 0
	global_load_dwordx4 v[16:19], v156, s[16:17] nt
	global_load_dwordx4 v[20:23], v157, s[16:17] nt
	global_load_dwordx4 v[24:27], v158, s[16:17] nt
	global_load_dwordx4 v[28:31], v159, s[16:17] nt
	s_add_u32 s16, s16, 0x4000
	s_addc_u32 s17, s17, 0
	s_nop 0
	global_load_dwordx4 v[32:35], v156, s[16:17] nt
	global_load_dwordx4 v[36:39], v157, s[16:17] nt
	global_load_dwordx4 v[40:43], v158, s[16:17] nt
	global_load_dwordx4 v[44:47], v159, s[16:17] nt
	s_add_u32 s16, s16, 0x4000
	s_addc_u32 s17, s17, 0
	s_nop 0
	global_load_dwordx4 v[48:51], v156, s[16:17] nt
	global_load_dwordx4 v[52:55], v157, s[16:17] nt
	global_load_dwordx4 v[56:59], v158, s[16:17] nt
	global_load_dwordx4 v[60:63], v159, s[16:17] nt
	s_waitcnt vmcnt(20)
	s_branch .Lp9c0_B_st

.Lp9c0_B_st:
	s_lshr_b32 s22, s4, 8
	s_and_b32 s23, s4, 0xff
	s_and_b32 s27, s22, 1
	s_lshr_b32 s22, s22, 1
	s_add_i32 s22, s22, 50
	s_mul_i32 s24, s22, 0x300000
	s_lshr_b32 s25, s23, 5
	s_lshl_b32 s25, s25, 7
	s_add_i32 s24, s24, s25
	s_and_b32 s26, s23, 31
	s_lshr_b32 s25, s26, 2
	s_lshl_b32 s25, s25, 18
	s_add_i32 s24, s24, s25
	s_lshl_b32 s25, s27, 17
	s_add_i32 s24, s24, s25
	s_and_b32 s25, s26, 3
	s_lshl_b32 s25, s25, 15
	s_add_i32 s24, s24, s25
	s_add_u32 s20, s10, s24
	s_addc_u32 s21, s11, 0
	v_mul_f32_e32 v64, 0x42000000, v64
	v_mul_f32_e32 v68, 0x42000000, v68
	v_mul_f32_e32 v72, 0x42000000, v72
	v_mul_f32_e32 v76, 0x42000000, v76
	v_mul_f32_e32 v80, 0x42000000, v80
	v_mul_f32_e32 v84, 0x42000000, v84
	v_mul_f32_e32 v88, 0x42000000, v88
	v_mul_f32_e32 v92, 0x42000000, v92
	v_mul_f32_e32 v96, 0x42000000, v96
	v_mul_f32_e32 v100, 0x42000000, v100
	v_mul_f32_e32 v104, 0x42000000, v104
	v_mul_f32_e32 v108, 0x42000000, v108
	v_mul_f32_e32 v112, 0x42000000, v112
	v_mul_f32_e32 v116, 0x42000000, v116
	v_mul_f32_e32 v120, 0x42000000, v120
	v_mul_f32_e32 v124, 0x42000000, v124
	v_med3_f32 v64, v64, s28, v161
	v_med3_f32 v68, v68, s28, v161
	v_med3_f32 v72, v72, s28, v161
	v_med3_f32 v76, v76, s28, v161
	v_med3_f32 v80, v80, s28, v161
	v_med3_f32 v84, v84, s28, v161
	v_med3_f32 v88, v88, s28, v161
	v_med3_f32 v92, v92, s28, v161
	v_med3_f32 v96, v96, s28, v161
	v_med3_f32 v100, v100, s28, v161
	v_med3_f32 v104, v104, s28, v161
	v_med3_f32 v108, v108, s28, v161
	v_med3_f32 v112, v112, s28, v161
	v_med3_f32 v116, v116, s28, v161
	v_med3_f32 v120, v120, s28, v161
	v_med3_f32 v124, v124, s28, v161
	v_cvt_pk_fp8_f32 v148, v64, v68
	v_cvt_pk_fp8_f32 v149, v80, v84
	v_cvt_pk_fp8_f32 v150, v96, v100
	v_cvt_pk_fp8_f32 v151, v112, v116
	v_cvt_pk_fp8_f32 v148, v72, v76 op_sel:[0,0,1]
	v_cvt_pk_fp8_f32 v149, v88, v92 op_sel:[0,0,1]
	v_cvt_pk_fp8_f32 v150, v104, v108 op_sel:[0,0,1]
	v_cvt_pk_fp8_f32 v151, v120, v124 op_sel:[0,0,1]
	s_nop 0
	global_store_dwordx4 v160, v[148:151], s[20:21]
	v_mul_f32_e32 v65, 0x42000000, v65
	v_mul_f32_e32 v69, 0x42000000, v69
	v_mul_f32_e32 v73, 0x42000000, v73
	v_mul_f32_e32 v77, 0x42000000, v77
	v_mul_f32_e32 v81, 0x42000000, v81
	v_mul_f32_e32 v85, 0x42000000, v85
	v_mul_f32_e32 v89, 0x42000000, v89
	v_mul_f32_e32 v93, 0x42000000, v93
	v_mul_f32_e32 v97, 0x42000000, v97
	v_mul_f32_e32 v101, 0x42000000, v101
	v_mul_f32_e32 v105, 0x42000000, v105
	v_mul_f32_e32 v109, 0x42000000, v109
	v_mul_f32_e32 v113, 0x42000000, v113
	v_mul_f32_e32 v117, 0x42000000, v117
	v_mul_f32_e32 v121, 0x42000000, v121
	v_mul_f32_e32 v125, 0x42000000, v125
	v_med3_f32 v65, v65, s28, v161
	v_med3_f32 v69, v69, s28, v161
	v_med3_f32 v73, v73, s28, v161
	v_med3_f32 v77, v77, s28, v161
	v_med3_f32 v81, v81, s28, v161
	v_med3_f32 v85, v85, s28, v161
	v_med3_f32 v89, v89, s28, v161
	v_med3_f32 v93, v93, s28, v161
	v_med3_f32 v97, v97, s28, v161
	v_med3_f32 v101, v101, s28, v161
	v_med3_f32 v105, v105, s28, v161
	v_med3_f32 v109, v109, s28, v161
	v_med3_f32 v113, v113, s28, v161
	v_med3_f32 v117, v117, s28, v161
	v_med3_f32 v121, v121, s28, v161
	v_med3_f32 v125, v125, s28, v161
	v_cvt_pk_fp8_f32 v152, v65, v69
	v_cvt_pk_fp8_f32 v153, v81, v85
	v_cvt_pk_fp8_f32 v154, v97, v101
	v_cvt_pk_fp8_f32 v155, v113, v117
	v_cvt_pk_fp8_f32 v152, v73, v77 op_sel:[0,0,1]
	v_cvt_pk_fp8_f32 v153, v89, v93 op_sel:[0,0,1]
	v_cvt_pk_fp8_f32 v154, v105, v109 op_sel:[0,0,1]
	v_cvt_pk_fp8_f32 v155, v121, v125 op_sel:[0,0,1]
	s_nop 0
	global_store_dwordx4 v160, v[152:155], s[20:21] offset:1024
	v_mul_f32_e32 v66, 0x42000000, v66
	v_mul_f32_e32 v70, 0x42000000, v70
	v_mul_f32_e32 v74, 0x42000000, v74
	v_mul_f32_e32 v78, 0x42000000, v78
	v_mul_f32_e32 v82, 0x42000000, v82
	v_mul_f32_e32 v86, 0x42000000, v86
	v_mul_f32_e32 v90, 0x42000000, v90
	v_mul_f32_e32 v94, 0x42000000, v94
	v_mul_f32_e32 v98, 0x42000000, v98
	v_mul_f32_e32 v102, 0x42000000, v102
	v_mul_f32_e32 v106, 0x42000000, v106
	v_mul_f32_e32 v110, 0x42000000, v110
	v_mul_f32_e32 v114, 0x42000000, v114
	v_mul_f32_e32 v118, 0x42000000, v118
	v_mul_f32_e32 v122, 0x42000000, v122
	v_mul_f32_e32 v126, 0x42000000, v126
	v_med3_f32 v66, v66, s28, v161
	v_med3_f32 v70, v70, s28, v161
	v_med3_f32 v74, v74, s28, v161
	v_med3_f32 v78, v78, s28, v161
	v_med3_f32 v82, v82, s28, v161
	v_med3_f32 v86, v86, s28, v161
	v_med3_f32 v90, v90, s28, v161
	v_med3_f32 v94, v94, s28, v161
	v_med3_f32 v98, v98, s28, v161
	v_med3_f32 v102, v102, s28, v161
	v_med3_f32 v106, v106, s28, v161
	v_med3_f32 v110, v110, s28, v161
	v_med3_f32 v114, v114, s28, v161
	v_med3_f32 v118, v118, s28, v161
	v_med3_f32 v122, v122, s28, v161
	v_med3_f32 v126, v126, s28, v161
	v_cvt_pk_fp8_f32 v148, v66, v70
	v_cvt_pk_fp8_f32 v149, v82, v86
	v_cvt_pk_fp8_f32 v150, v98, v102
	v_cvt_pk_fp8_f32 v151, v114, v118
	v_cvt_pk_fp8_f32 v148, v74, v78 op_sel:[0,0,1]
	v_cvt_pk_fp8_f32 v149, v90, v94 op_sel:[0,0,1]
	v_cvt_pk_fp8_f32 v150, v106, v110 op_sel:[0,0,1]
	v_cvt_pk_fp8_f32 v151, v122, v126 op_sel:[0,0,1]
	s_nop 0
	global_store_dwordx4 v160, v[148:151], s[20:21] offset:2048
	v_mul_f32_e32 v67, 0x42000000, v67
	v_mul_f32_e32 v71, 0x42000000, v71
	v_mul_f32_e32 v75, 0x42000000, v75
	v_mul_f32_e32 v79, 0x42000000, v79
	v_mul_f32_e32 v83, 0x42000000, v83
	v_mul_f32_e32 v87, 0x42000000, v87
	v_mul_f32_e32 v91, 0x42000000, v91
	v_mul_f32_e32 v95, 0x42000000, v95
	v_mul_f32_e32 v99, 0x42000000, v99
	v_mul_f32_e32 v103, 0x42000000, v103
	v_mul_f32_e32 v107, 0x42000000, v107
	v_mul_f32_e32 v111, 0x42000000, v111
	v_mul_f32_e32 v115, 0x42000000, v115
	v_mul_f32_e32 v119, 0x42000000, v119
	v_mul_f32_e32 v123, 0x42000000, v123
	v_mul_f32_e32 v127, 0x42000000, v127
	v_med3_f32 v67, v67, s28, v161
	v_med3_f32 v71, v71, s28, v161
	v_med3_f32 v75, v75, s28, v161
	v_med3_f32 v79, v79, s28, v161
	v_med3_f32 v83, v83, s28, v161
	v_med3_f32 v87, v87, s28, v161
	v_med3_f32 v91, v91, s28, v161
	v_med3_f32 v95, v95, s28, v161
	v_med3_f32 v99, v99, s28, v161
	v_med3_f32 v103, v103, s28, v161
	v_med3_f32 v107, v107, s28, v161
	v_med3_f32 v111, v111, s28, v161
	v_med3_f32 v115, v115, s28, v161
	v_med3_f32 v119, v119, s28, v161
	v_med3_f32 v123, v123, s28, v161
	v_med3_f32 v127, v127, s28, v161
	v_cvt_pk_fp8_f32 v152, v67, v71
	v_cvt_pk_fp8_f32 v153, v83, v87
	v_cvt_pk_fp8_f32 v154, v99, v103
	v_cvt_pk_fp8_f32 v155, v115, v119
	v_cvt_pk_fp8_f32 v152, v75, v79 op_sel:[0,0,1]
	v_cvt_pk_fp8_f32 v153, v91, v95 op_sel:[0,0,1]
	v_cvt_pk_fp8_f32 v154, v107, v111 op_sel:[0,0,1]
	v_cvt_pk_fp8_f32 v155, v123, v127 op_sel:[0,0,1]
	s_nop 0
	global_store_dwordx4 v160, v[152:155], s[20:21] offset:3072
	s_cmp_ge_u32 s7, s6
	s_cbranch_scc1 .Lp9c0_done
	s_mov_b32 s4, s7
	s_add_i32 s7, s4, s5
	s_cmp_lt_u32 s7, s6
	s_cbranch_scc0 .Lp9c0_A_last
	s_lshr_b32 s22, s7, 8
	s_and_b32 s23, s7, 0xff
	s_and_b32 s27, s22, 1
	s_lshr_b32 s22, s22, 1
	s_cmp_eq_u32 s27, 0
	s_cselect_b64 s[16:17], s[12:13], s[14:15]
	s_add_i32 s22, s22, 50
	s_lshl_b32 s24, s22, 22
	s_lshr_b32 s25, s23, 5
	s_lshl_b32 s25, s25, 19
	s_and_b32 s26, s23, 31
	s_lshl_b32 s26, s26, 7
	s_add_i32 s24, s24, s25
	s_add_i32 s24, s24, s26
	s_add_u32 s16, s16, s24
	s_addc_u32 s17, s17, 0
	s_nop 0
	global_load_dwordx4 v[64:67], v156, s[16:17] nt
	global_load_dwordx4 v[68:71], v157, s[16:17] nt
	global_load_dwordx4 v[72:75], v158, s[16:17] nt
	global_load_dwordx4 v[76:79], v159, s[16:17] nt
	s_add_u32 s16, s16, 0x4000
	s_addc_u32 s17, s17, 0
	s_nop 0
	global_load_dwordx4 v[80:83], v156, s[16:17] nt
	global_load_dwordx4 v[84:87], v157, s[16:17] nt
	global_load_dwordx4 v[88:91], v158, s[16:17] nt
	global_load_dwordx4 v[92:95], v159, s[16:17] nt
	s_add_u32 s16, s16, 0x4000
	s_addc_u32 s17, s17, 0
	s_nop 0
	global_load_dwordx4 v[96:99], v156, s[16:17] nt
	global_load_dwordx4 v[100:103], v157, s[16:17] nt
	global_load_dwordx4 v[104:107], v158, s[16:17] nt
	global_load_dwordx4 v[108:111], v159, s[16:17] nt
	s_add_u32 s16, s16, 0x4000
	s_addc_u32 s17, s17, 0
	s_nop 0
	global_load_dwordx4 v[112:115], v156, s[16:17] nt
	global_load_dwordx4 v[116:119], v157, s[16:17] nt
	global_load_dwordx4 v[120:123], v158, s[16:17] nt
	global_load_dwordx4 v[124:127], v159, s[16:17] nt
	s_waitcnt vmcnt(20)
	s_branch .Lp9c0_A_st

.Lp9c0_A_st:
	s_lshr_b32 s22, s4, 8
	s_and_b32 s23, s4, 0xff
	s_and_b32 s27, s22, 1
	s_lshr_b32 s22, s22, 1
	s_add_i32 s22, s22, 50
	s_mul_i32 s24, s22, 0x300000
	s_lshr_b32 s25, s23, 5
	s_lshl_b32 s25, s25, 7
	s_add_i32 s24, s24, s25
	s_and_b32 s26, s23, 31
	s_lshr_b32 s25, s26, 2
	s_lshl_b32 s25, s25, 18
	s_add_i32 s24, s24, s25
	s_lshl_b32 s25, s27, 17
	s_add_i32 s24, s24, s25
	s_and_b32 s25, s26, 3
	s_lshl_b32 s25, s25, 15
	s_add_i32 s24, s24, s25
	s_add_u32 s20, s10, s24
	s_addc_u32 s21, s11, 0
	v_mul_f32_e32 v0, 0x42000000, v0
	v_mul_f32_e32 v4, 0x42000000, v4
	v_mul_f32_e32 v8, 0x42000000, v8
	v_mul_f32_e32 v12, 0x42000000, v12
	v_mul_f32_e32 v16, 0x42000000, v16
	v_mul_f32_e32 v20, 0x42000000, v20
	v_mul_f32_e32 v24, 0x42000000, v24
	v_mul_f32_e32 v28, 0x42000000, v28
	v_mul_f32_e32 v32, 0x42000000, v32
	v_mul_f32_e32 v36, 0x42000000, v36
	v_mul_f32_e32 v40, 0x42000000, v40
	v_mul_f32_e32 v44, 0x42000000, v44
	v_mul_f32_e32 v48, 0x42000000, v48
	v_mul_f32_e32 v52, 0x42000000, v52
	v_mul_f32_e32 v56, 0x42000000, v56
	v_mul_f32_e32 v60, 0x42000000, v60
	v_med3_f32 v0, v0, s28, v161
	v_med3_f32 v4, v4, s28, v161
	v_med3_f32 v8, v8, s28, v161
	v_med3_f32 v12, v12, s28, v161
	v_med3_f32 v16, v16, s28, v161
	v_med3_f32 v20, v20, s28, v161
	v_med3_f32 v24, v24, s28, v161
	v_med3_f32 v28, v28, s28, v161
	v_med3_f32 v32, v32, s28, v161
	v_med3_f32 v36, v36, s28, v161
	v_med3_f32 v40, v40, s28, v161
	v_med3_f32 v44, v44, s28, v161
	v_med3_f32 v48, v48, s28, v161
	v_med3_f32 v52, v52, s28, v161
	v_med3_f32 v56, v56, s28, v161
	v_med3_f32 v60, v60, s28, v161
	v_cvt_pk_fp8_f32 v148, v0, v4
	v_cvt_pk_fp8_f32 v149, v16, v20
	v_cvt_pk_fp8_f32 v150, v32, v36
	v_cvt_pk_fp8_f32 v151, v48, v52
	v_cvt_pk_fp8_f32 v148, v8, v12 op_sel:[0,0,1]
	v_cvt_pk_fp8_f32 v149, v24, v28 op_sel:[0,0,1]
	v_cvt_pk_fp8_f32 v150, v40, v44 op_sel:[0,0,1]
	v_cvt_pk_fp8_f32 v151, v56, v60 op_sel:[0,0,1]
	s_nop 0
	global_store_dwordx4 v160, v[148:151], s[20:21]
	v_mul_f32_e32 v1, 0x42000000, v1
	v_mul_f32_e32 v5, 0x42000000, v5
	v_mul_f32_e32 v9, 0x42000000, v9
	v_mul_f32_e32 v13, 0x42000000, v13
	v_mul_f32_e32 v17, 0x42000000, v17
	v_mul_f32_e32 v21, 0x42000000, v21
	v_mul_f32_e32 v25, 0x42000000, v25
	v_mul_f32_e32 v29, 0x42000000, v29
	v_mul_f32_e32 v33, 0x42000000, v33
	v_mul_f32_e32 v37, 0x42000000, v37
	v_mul_f32_e32 v41, 0x42000000, v41
	v_mul_f32_e32 v45, 0x42000000, v45
	v_mul_f32_e32 v49, 0x42000000, v49
	v_mul_f32_e32 v53, 0x42000000, v53
	v_mul_f32_e32 v57, 0x42000000, v57
	v_mul_f32_e32 v61, 0x42000000, v61
	v_med3_f32 v1, v1, s28, v161
	v_med3_f32 v5, v5, s28, v161
	v_med3_f32 v9, v9, s28, v161
	v_med3_f32 v13, v13, s28, v161
	v_med3_f32 v17, v17, s28, v161
	v_med3_f32 v21, v21, s28, v161
	v_med3_f32 v25, v25, s28, v161
	v_med3_f32 v29, v29, s28, v161
	v_med3_f32 v33, v33, s28, v161
	v_med3_f32 v37, v37, s28, v161
	v_med3_f32 v41, v41, s28, v161
	v_med3_f32 v45, v45, s28, v161
	v_med3_f32 v49, v49, s28, v161
	v_med3_f32 v53, v53, s28, v161
	v_med3_f32 v57, v57, s28, v161
	v_med3_f32 v61, v61, s28, v161
	v_cvt_pk_fp8_f32 v152, v1, v5
	v_cvt_pk_fp8_f32 v153, v17, v21
	v_cvt_pk_fp8_f32 v154, v33, v37
	v_cvt_pk_fp8_f32 v155, v49, v53
	v_cvt_pk_fp8_f32 v152, v9, v13 op_sel:[0,0,1]
	v_cvt_pk_fp8_f32 v153, v25, v29 op_sel:[0,0,1]
	v_cvt_pk_fp8_f32 v154, v41, v45 op_sel:[0,0,1]
	v_cvt_pk_fp8_f32 v155, v57, v61 op_sel:[0,0,1]
	s_nop 0
	global_store_dwordx4 v160, v[152:155], s[20:21] offset:1024
	v_mul_f32_e32 v2, 0x42000000, v2
	v_mul_f32_e32 v6, 0x42000000, v6
	v_mul_f32_e32 v10, 0x42000000, v10
	v_mul_f32_e32 v14, 0x42000000, v14
	v_mul_f32_e32 v18, 0x42000000, v18
	v_mul_f32_e32 v22, 0x42000000, v22
	v_mul_f32_e32 v26, 0x42000000, v26
	v_mul_f32_e32 v30, 0x42000000, v30
	v_mul_f32_e32 v34, 0x42000000, v34
	v_mul_f32_e32 v38, 0x42000000, v38
	v_mul_f32_e32 v42, 0x42000000, v42
	v_mul_f32_e32 v46, 0x42000000, v46
	v_mul_f32_e32 v50, 0x42000000, v50
	v_mul_f32_e32 v54, 0x42000000, v54
	v_mul_f32_e32 v58, 0x42000000, v58
	v_mul_f32_e32 v62, 0x42000000, v62
	v_med3_f32 v2, v2, s28, v161
	v_med3_f32 v6, v6, s28, v161
	v_med3_f32 v10, v10, s28, v161
	v_med3_f32 v14, v14, s28, v161
	v_med3_f32 v18, v18, s28, v161
	v_med3_f32 v22, v22, s28, v161
	v_med3_f32 v26, v26, s28, v161
	v_med3_f32 v30, v30, s28, v161
	v_med3_f32 v34, v34, s28, v161
	v_med3_f32 v38, v38, s28, v161
	v_med3_f32 v42, v42, s28, v161
	v_med3_f32 v46, v46, s28, v161
	v_med3_f32 v50, v50, s28, v161
	v_med3_f32 v54, v54, s28, v161
	v_med3_f32 v58, v58, s28, v161
	v_med3_f32 v62, v62, s28, v161
	v_cvt_pk_fp8_f32 v148, v2, v6
	v_cvt_pk_fp8_f32 v149, v18, v22
	v_cvt_pk_fp8_f32 v150, v34, v38
	v_cvt_pk_fp8_f32 v151, v50, v54
	v_cvt_pk_fp8_f32 v148, v10, v14 op_sel:[0,0,1]
	v_cvt_pk_fp8_f32 v149, v26, v30 op_sel:[0,0,1]
	v_cvt_pk_fp8_f32 v150, v42, v46 op_sel:[0,0,1]
	v_cvt_pk_fp8_f32 v151, v58, v62 op_sel:[0,0,1]
	s_nop 0
	global_store_dwordx4 v160, v[148:151], s[20:21] offset:2048
	v_mul_f32_e32 v3, 0x42000000, v3
	v_mul_f32_e32 v7, 0x42000000, v7
	v_mul_f32_e32 v11, 0x42000000, v11
	v_mul_f32_e32 v15, 0x42000000, v15
	v_mul_f32_e32 v19, 0x42000000, v19
	v_mul_f32_e32 v23, 0x42000000, v23
	v_mul_f32_e32 v27, 0x42000000, v27
	v_mul_f32_e32 v31, 0x42000000, v31
	v_mul_f32_e32 v35, 0x42000000, v35
	v_mul_f32_e32 v39, 0x42000000, v39
	v_mul_f32_e32 v43, 0x42000000, v43
	v_mul_f32_e32 v47, 0x42000000, v47
	v_mul_f32_e32 v51, 0x42000000, v51
	v_mul_f32_e32 v55, 0x42000000, v55
	v_mul_f32_e32 v59, 0x42000000, v59
	v_mul_f32_e32 v63, 0x42000000, v63
	v_med3_f32 v3, v3, s28, v161
	v_med3_f32 v7, v7, s28, v161
	v_med3_f32 v11, v11, s28, v161
	v_med3_f32 v15, v15, s28, v161
	v_med3_f32 v19, v19, s28, v161
	v_med3_f32 v23, v23, s28, v161
	v_med3_f32 v27, v27, s28, v161
	v_med3_f32 v31, v31, s28, v161
	v_med3_f32 v35, v35, s28, v161
	v_med3_f32 v39, v39, s28, v161
	v_med3_f32 v43, v43, s28, v161
	v_med3_f32 v47, v47, s28, v161
	v_med3_f32 v51, v51, s28, v161
	v_med3_f32 v55, v55, s28, v161
	v_med3_f32 v59, v59, s28, v161
	v_med3_f32 v63, v63, s28, v161
	v_cvt_pk_fp8_f32 v152, v3, v7
	v_cvt_pk_fp8_f32 v153, v19, v23
	v_cvt_pk_fp8_f32 v154, v35, v39
	v_cvt_pk_fp8_f32 v155, v51, v55
	v_cvt_pk_fp8_f32 v152, v11, v15 op_sel:[0,0,1]
	v_cvt_pk_fp8_f32 v153, v27, v31 op_sel:[0,0,1]
	v_cvt_pk_fp8_f32 v154, v43, v47 op_sel:[0,0,1]
	v_cvt_pk_fp8_f32 v155, v59, v63 op_sel:[0,0,1]
	s_nop 0
	global_store_dwordx4 v160, v[152:155], s[20:21] offset:3072
	s_cmp_ge_u32 s7, s6
	s_cbranch_scc1 .Lp9c0_done
	s_mov_b32 s4, s7
	s_branch .Lp9c0_loop
